# adds: p4_ret cross+inner stage LDS fragment reads software-pipelined (3-4 deep), P1 conversion queue rewritten (chunks of 4 adjacent tiles, 2 tiles of loads in flight)
# baseline (speedup 1.0000x reference)
; __device__ __forceinline__ Cvb conv8b_dec(const Ctx& X, int bit) { Cvb c; int kb, nb;
;     if (bit < I_GU8 / 8) { const int e = bit >> 8, r = bit & 255; kb = r >> 4; nb = r & 15; c.N = 2 * DFF; c.W = XP_w_gu(X) + (size_t)e * D * (2 * DFF); c.WT = XP_WguT(X) + (size_t)e * 16 * PAN_GU + (size_t)kb * PAN_GU; }
;     else { const int b2 = bit - I_GU8 / 8, e = b2 >> 7, r = b2 & 127; kb = r >> 3; nb = r & 7; c.N = D; c.W = XP_w_d(X) + (size_t)e * DFF * D; c.WT = XP_WdT(X) + (size_t)e * 16 * PAN_D + (size_t)kb * PAN_D; }
;     c.W += (size_t)(kb * 128 + 16 * X.wave) * c.N + nb * 256 + 4 * X.lane;
;     c.WT += (size_t)(nb * 256 + 32 * X.wave + (X.lane >> 3)) * 128 + 16 * (X.lane & 7);
;     return c; }
; __device__ __forceinline__ void conv8b_run(const Ctx& X, int first, int step, int count) {
;     if (count <= 0) return;
;     f32x4 v[16];
;     Cvb c = conv8b_dec(X, first), cn = c;
; #pragma unroll
;     for (int i = 0; i < 16; ++i) v[i] = __builtin_nontemporal_load((const f32x4*)(c.W + (size_t)i * c.N));
; #pragma unroll 1
;     for (int j = 0; j < count; ++j) {
;         LAS uchar* buf = X.lds + (j & 1) * CVT_BUF;
; #pragma unroll
;         for (int q = 0; q < 4; ++q) { u32x4 o;
;             o.x = pk_fp8x4(v[0][q] * W8_SCALE, v[1][q] * W8_SCALE, v[2][q] * W8_SCALE, v[3][q] * W8_SCALE); o.y = pk_fp8x4(v[4][q] * W8_SCALE, v[5][q] * W8_SCALE, v[6][q] * W8_SCALE, v[7][q] * W8_SCALE);
;             o.z = pk_fp8x4(v[8][q] * W8_SCALE, v[9][q] * W8_SCALE, v[10][q] * W8_SCALE, v[11][q] * W8_SCALE); o.w = pk_fp8x4(v[12][q] * W8_SCALE, v[13][q] * W8_SCALE, v[14][q] * W8_SCALE, v[15][q] * W8_SCALE);
;             *(LAS u32x4*)(buf + (4 * X.lane + q) * CVT_STRIDE + 16 * X.wave) = o; }
;         if (j + 1 < count) { cn = conv8b_dec(X, first + (j + 1) * step);
; #pragma unroll
;             for (int i = 0; i < 16; ++i) v[i] = __builtin_nontemporal_load((const f32x4*)(cn.W + (size_t)i * cn.N)); }
;         asm volatile("s_waitcnt lgkmcnt(0)" ::: "memory"); __builtin_amdgcn_s_barrier();
; #pragma unroll
;         for (int it = 0; it < 4; ++it) { const u32x4 r = *(const LAS u32x4*)(buf + (32 * X.wave + 8 * it + (X.lane >> 3)) * CVT_STRIDE + 16 * (X.lane & 7));
;             __builtin_nontemporal_store(r, (u32x4*)(c.WT + (size_t)it * 8 * 128)); }
;         c = cn;
;     }
;     asm volatile("s_waitcnt lgkmcnt(0)" ::: "memory"); __builtin_amdgcn_s_barrier();
; }
.LBB0_122:
	v_cmp_eq_u32_e64 s[2:3], 0, v0
	s_waitcnt vmcnt(0)
	s_mov_b32 s10, 0xee00
	s_and_b64 s[6:7], s[6:7], exec
	s_cselect_b32 s28, s10, 0x18000
	v_mov_b32_e32 v154, s90
	v_mov_b32_e32 v155, s91
	v_add_co_u32_e32 v154, vcc, 0x14000, v154
	s_nop 1
	v_addc_co_u32_e32 v155, vcc, 0, v155, vcc
	v_mov_b32_e32 v157, 32
	v_mov_b32_e32 v156, 0x23040
	v_mov_b32_e32 v153, 0
	s_and_saveexec_b64 s[22:23], s[2:3]
	s_cbranch_execz .Lcq1_q0
	global_atomic_add v153, v[154:155], v157, off sc0
.Lcq1_q0:
	s_or_b64 exec, exec, s[22:23]
	s_load_dwordx2 s[6:7], s[0:1], 0x70
	s_load_dwordx2 s[8:9], s[0:1], 0x80
	s_mov_b32 s24, 0xc3e00000
	v_mov_b32_e32 v150, 0x43e00000
	v_lshlrev_b32_e32 v146, 4, v194
	v_mul_u32_u24_e32 v147, 0x240, v194
	s_lshl_b32 s20, s93, 4
	v_add_u32_e32 v147, s20, v147
	v_lshrrev_b32_e32 v151, 3, v194
	s_lshl_b32 s20, s93, 5
	v_add_u32_e32 v152, s20, v151
	v_mul_u32_u24_e32 v148, 0x90, v152
	v_and_b32_e32 v152, 7, v194
	v_lshl_add_u32 v148, v152, 4, v148
	v_lshlrev_b32_e32 v151, 7, v151
	v_lshl_add_u32 v149, v152, 4, v151
	s_waitcnt lgkmcnt(0)
.Lcq1_outer:
	s_and_saveexec_b64 s[22:23], s[2:3]
	s_cbranch_execz .Lcq1_qa
	s_waitcnt vmcnt(0)
	ds_write_b32 v156, v153
.Lcq1_qa:
	s_or_b64 exec, exec, s[22:23]
	s_waitcnt lgkmcnt(0)
	s_barrier
	ds_read_b32 v151, v156
	s_waitcnt lgkmcnt(0)
	v_readfirstlane_b32 s29, v151
	s_cmp_ge_i32 s29, s28
	s_cbranch_scc1 .Lcq1_qdone
	s_and_saveexec_b64 s[22:23], s[2:3]
	s_cbranch_execz .Lcq1_qb
	global_atomic_add v153, v[154:155], v157, off sc0
.Lcq1_qb:
	s_or_b64 exec, exec, s[22:23]
	s_lshr_b32 s18, s29, 3
	s_mov_b32 s19, 4
	s_add_i32 s27, s18, 1
	s_cmp_lt_u32 s18, 0x2000
	s_cbranch_scc0 .Lcq1_dnP0
	s_lshr_b32 s20, s18, 4
	s_lshl_b32 s20, s20, 21
	s_and_b32 s21, s18, 15
	s_lshl_b32 s21, s21, 10
	s_add_u32 s20, s20, s21
	s_lshl_b32 s21, s93, 18
	s_add_u32 s20, s20, s21
	s_add_u32 s10, s6, s20
	s_addc_u32 s11, s7, 0
	s_movk_i32 s12, 0x4000
	s_lshl_b32 s20, s18, 15
	s_add_u32 s20, s20, 0x30000000
	s_branch .Lcq1_cmP0
.Lcq1_dnP0:
	s_sub_u32 s22, s18, 0x2000
	s_lshr_b32 s20, s22, 3
	s_lshl_b32 s20, s20, 20
	s_and_b32 s21, s22, 7
	s_lshl_b32 s21, s21, 10
	s_add_u32 s20, s20, s21
	s_lshl_b32 s21, s93, 17
	s_add_u32 s20, s20, s21
	s_add_u32 s10, s8, s20
	s_addc_u32 s11, s9, 0
	s_movk_i32 s12, 0x2000
	s_lshl_b32 s20, s22, 15
	s_add_u32 s20, s20, 0x50000000
.Lcq1_cmP0:
	s_lshl_b32 s21, s93, 12
	s_add_u32 s20, s20, s21
	s_add_u32 s14, s90, s20
	s_addc_u32 s15, s91, 0
	global_load_dwordx4 v[2:5], v146, s[10:11] nt
	s_add_u32 s10, s10, s12
	s_addc_u32 s11, s11, 0
	global_load_dwordx4 v[6:9], v146, s[10:11] nt
	s_add_u32 s10, s10, s12
	s_addc_u32 s11, s11, 0
	global_load_dwordx4 v[10:13], v146, s[10:11] nt
	s_add_u32 s10, s10, s12
	s_addc_u32 s11, s11, 0
	global_load_dwordx4 v[14:17], v146, s[10:11] nt
	s_add_u32 s10, s10, s12
	s_addc_u32 s11, s11, 0
	global_load_dwordx4 v[18:21], v146, s[10:11] nt
	s_add_u32 s10, s10, s12
	s_addc_u32 s11, s11, 0
	global_load_dwordx4 v[22:25], v146, s[10:11] nt
	s_add_u32 s10, s10, s12
	s_addc_u32 s11, s11, 0
	global_load_dwordx4 v[26:29], v146, s[10:11] nt
	s_add_u32 s10, s10, s12
	s_addc_u32 s11, s11, 0
	global_load_dwordx4 v[30:33], v146, s[10:11] nt
	s_add_u32 s10, s10, s12
	s_addc_u32 s11, s11, 0
	global_load_dwordx4 v[34:37], v146, s[10:11] nt
	s_add_u32 s10, s10, s12
	s_addc_u32 s11, s11, 0
	global_load_dwordx4 v[38:41], v146, s[10:11] nt
	s_add_u32 s10, s10, s12
	s_addc_u32 s11, s11, 0
	global_load_dwordx4 v[42:45], v146, s[10:11] nt
	s_add_u32 s10, s10, s12
	s_addc_u32 s11, s11, 0
	global_load_dwordx4 v[46:49], v146, s[10:11] nt
	s_add_u32 s10, s10, s12
	s_addc_u32 s11, s11, 0
	global_load_dwordx4 v[50:53], v146, s[10:11] nt
	s_add_u32 s10, s10, s12
	s_addc_u32 s11, s11, 0
	global_load_dwordx4 v[54:57], v146, s[10:11] nt
	s_add_u32 s10, s10, s12
	s_addc_u32 s11, s11, 0
	global_load_dwordx4 v[58:61], v146, s[10:11] nt
	s_add_u32 s10, s10, s12
	s_addc_u32 s11, s11, 0
	global_load_dwordx4 v[62:65], v146, s[10:11] nt
	s_add_i32 s18, s18, 2
	s_add_i32 s19, s19, -1
	s_mov_b32 s25, 0
	s_cmp_eq_u32 s19, 0
	s_cbranch_scc1 .Lcq1_loop
	s_cmp_lt_u32 s27, 0x2000
	s_cbranch_scc0 .Lcq1_dnP1
	s_lshr_b32 s20, s27, 4
	s_lshl_b32 s20, s20, 21
	s_and_b32 s21, s27, 15
	s_lshl_b32 s21, s21, 10
	s_add_u32 s20, s20, s21
	s_lshl_b32 s21, s93, 18
	s_add_u32 s20, s20, s21
	s_add_u32 s10, s6, s20
	s_addc_u32 s11, s7, 0
	s_movk_i32 s12, 0x4000
	s_lshl_b32 s20, s27, 15
	s_add_u32 s20, s20, 0x30000000
	s_branch .Lcq1_cmP1
.Lcq1_dnP1:
	s_sub_u32 s22, s27, 0x2000
	s_lshr_b32 s20, s22, 3
	s_lshl_b32 s20, s20, 20
	s_and_b32 s21, s22, 7
	s_lshl_b32 s21, s21, 10
	s_add_u32 s20, s20, s21
	s_lshl_b32 s21, s93, 17
	s_add_u32 s20, s20, s21
	s_add_u32 s10, s8, s20
	s_addc_u32 s11, s9, 0
	s_movk_i32 s12, 0x2000
	s_lshl_b32 s20, s22, 15
	s_add_u32 s20, s20, 0x50000000
.Lcq1_cmP1:
	s_lshl_b32 s21, s93, 12
	s_add_u32 s20, s20, s21
	s_add_u32 s16, s90, s20
	s_addc_u32 s17, s91, 0
	global_load_dwordx4 v[66:69], v146, s[10:11] nt
	s_add_u32 s10, s10, s12
	s_addc_u32 s11, s11, 0
	global_load_dwordx4 v[70:73], v146, s[10:11] nt
	s_add_u32 s10, s10, s12
	s_addc_u32 s11, s11, 0
	global_load_dwordx4 v[74:77], v146, s[10:11] nt
	s_add_u32 s10, s10, s12
	s_addc_u32 s11, s11, 0
	global_load_dwordx4 v[78:81], v146, s[10:11] nt
	s_add_u32 s10, s10, s12
	s_addc_u32 s11, s11, 0
	global_load_dwordx4 v[82:85], v146, s[10:11] nt
	s_add_u32 s10, s10, s12
	s_addc_u32 s11, s11, 0
	global_load_dwordx4 v[86:89], v146, s[10:11] nt
	s_add_u32 s10, s10, s12
	s_addc_u32 s11, s11, 0
	global_load_dwordx4 v[90:93], v146, s[10:11] nt
	s_add_u32 s10, s10, s12
	s_addc_u32 s11, s11, 0
	global_load_dwordx4 v[94:97], v146, s[10:11] nt
	s_add_u32 s10, s10, s12
	s_addc_u32 s11, s11, 0
	global_load_dwordx4 v[98:101], v146, s[10:11] nt
	s_add_u32 s10, s10, s12
	s_addc_u32 s11, s11, 0
	global_load_dwordx4 v[102:105], v146, s[10:11] nt
	s_add_u32 s10, s10, s12
	s_addc_u32 s11, s11, 0
	global_load_dwordx4 v[106:109], v146, s[10:11] nt
	s_add_u32 s10, s10, s12
	s_addc_u32 s11, s11, 0
	global_load_dwordx4 v[110:113], v146, s[10:11] nt
	s_add_u32 s10, s10, s12
	s_addc_u32 s11, s11, 0
	global_load_dwordx4 v[114:117], v146, s[10:11] nt
	s_add_u32 s10, s10, s12
	s_addc_u32 s11, s11, 0
	global_load_dwordx4 v[118:121], v146, s[10:11] nt
	s_add_u32 s10, s10, s12
	s_addc_u32 s11, s11, 0
	global_load_dwordx4 v[122:125], v146, s[10:11] nt
	s_add_u32 s10, s10, s12
	s_addc_u32 s11, s11, 0
	global_load_dwordx4 v[126:129], v146, s[10:11] nt
	s_add_i32 s27, s27, 2
	s_add_i32 s19, s19, -1
	s_mov_b32 s25, 1
	s_waitcnt vmcnt(16)
.Lcq1_loop:
	s_cmp_lg_u32 s25, 0
	s_cbranch_scc0 .Lcq1_w0A
	s_waitcnt vmcnt(20)
	s_branch .Lcq1_w1A

; #define LAS __attribute__((address_space(3)))
; __device__ __forceinline__ void conv8b_run(const Ctx& X, int first, int step, int count) {
;     ...
;         LAS uchar* buf = X.lds + (j & 1) * CVT_BUF;
; #pragma unroll
;         for (int q = 0; q < 4; ++q) { u32x4 o;
;             o.x = pk_fp8x4(v[0][q] * W8_SCALE, v[1][q] * W8_SCALE, v[2][q] * W8_SCALE, v[3][q] * W8_SCALE); o.y = pk_fp8x4(v[4][q] * W8_SCALE, v[5][q] * W8_SCALE, v[6][q] * W8_SCALE, v[7][q] * W8_SCALE);
;             o.z = pk_fp8x4(v[8][q] * W8_SCALE, v[9][q] * W8_SCALE, v[10][q] * W8_SCALE, v[11][q] * W8_SCALE); o.w = pk_fp8x4(v[12][q] * W8_SCALE, v[13][q] * W8_SCALE, v[14][q] * W8_SCALE, v[15][q] * W8_SCALE);
;             *(LAS u32x4*)(buf + (4 * X.lane + q) * CVT_STRIDE + 16 * X.wave) = o; }
;         if (j + 1 < count) { cn = conv8b_dec(X, first + (j + 1) * step);
; #pragma unroll
;             for (int i = 0; i < 16; ++i) v[i] = __builtin_nontemporal_load((const f32x4*)(cn.W + (size_t)i * cn.N)); }
;         asm volatile("s_waitcnt lgkmcnt(0)" ::: "memory"); __builtin_amdgcn_s_barrier();
; #pragma unroll
;         for (int it = 0; it < 4; ++it) { const u32x4 r = *(const LAS u32x4*)(buf + (32 * X.wave + 8 * it + (X.lane >> 3)) * CVT_STRIDE + 16 * (X.lane & 7));
;             __builtin_nontemporal_store(r, (u32x4*)(c.WT + (size_t)it * 8 * 128)); }
.Lcq1_w1A:
	v_mul_f32_e32 v2, 0x42800000, v2
	v_mul_f32_e32 v6, 0x42800000, v6
	v_med3_f32 v2, v2, s24, v150
	v_med3_f32 v6, v6, s24, v150
	v_mul_f32_e32 v10, 0x42800000, v10
	v_mul_f32_e32 v14, 0x42800000, v14
	v_cvt_pk_fp8_f32 v130, v2, v6
	v_med3_f32 v10, v10, s24, v150
	v_med3_f32 v14, v14, s24, v150
	v_cvt_pk_fp8_f32 v130, v10, v14 op_sel:[0,0,1]
	v_mul_f32_e32 v18, 0x42800000, v18
	v_mul_f32_e32 v22, 0x42800000, v22
	v_med3_f32 v18, v18, s24, v150
	v_med3_f32 v22, v22, s24, v150
	v_mul_f32_e32 v26, 0x42800000, v26
	v_mul_f32_e32 v30, 0x42800000, v30
	v_cvt_pk_fp8_f32 v131, v18, v22
	v_med3_f32 v26, v26, s24, v150
	v_med3_f32 v30, v30, s24, v150
	v_cvt_pk_fp8_f32 v131, v26, v30 op_sel:[0,0,1]
	v_mul_f32_e32 v34, 0x42800000, v34
	v_mul_f32_e32 v38, 0x42800000, v38
	v_med3_f32 v34, v34, s24, v150
	v_med3_f32 v38, v38, s24, v150
	v_mul_f32_e32 v42, 0x42800000, v42
	v_mul_f32_e32 v46, 0x42800000, v46
	v_cvt_pk_fp8_f32 v132, v34, v38
	v_med3_f32 v42, v42, s24, v150
	v_med3_f32 v46, v46, s24, v150
	v_cvt_pk_fp8_f32 v132, v42, v46 op_sel:[0,0,1]
	v_mul_f32_e32 v50, 0x42800000, v50
	v_mul_f32_e32 v54, 0x42800000, v54
	v_med3_f32 v50, v50, s24, v150
	v_med3_f32 v54, v54, s24, v150
	v_mul_f32_e32 v58, 0x42800000, v58
	v_mul_f32_e32 v62, 0x42800000, v62
	v_cvt_pk_fp8_f32 v133, v50, v54
	v_med3_f32 v58, v58, s24, v150
	v_med3_f32 v62, v62, s24, v150
	v_cvt_pk_fp8_f32 v133, v58, v62 op_sel:[0,0,1]
	s_nop 0
	ds_write_b128 v147, v[130:133] offset:0
	v_mul_f32_e32 v3, 0x42800000, v3
	v_mul_f32_e32 v7, 0x42800000, v7
	v_med3_f32 v3, v3, s24, v150
	v_med3_f32 v7, v7, s24, v150
	v_mul_f32_e32 v11, 0x42800000, v11
	v_mul_f32_e32 v15, 0x42800000, v15
	v_cvt_pk_fp8_f32 v134, v3, v7
	v_med3_f32 v11, v11, s24, v150
	v_med3_f32 v15, v15, s24, v150
	v_cvt_pk_fp8_f32 v134, v11, v15 op_sel:[0,0,1]
	v_mul_f32_e32 v19, 0x42800000, v19
	v_mul_f32_e32 v23, 0x42800000, v23
	v_med3_f32 v19, v19, s24, v150
	v_med3_f32 v23, v23, s24, v150
	v_mul_f32_e32 v27, 0x42800000, v27
	v_mul_f32_e32 v31, 0x42800000, v31
	v_cvt_pk_fp8_f32 v135, v19, v23
	v_med3_f32 v27, v27, s24, v150
	v_med3_f32 v31, v31, s24, v150
	v_cvt_pk_fp8_f32 v135, v27, v31 op_sel:[0,0,1]
	v_mul_f32_e32 v35, 0x42800000, v35
	v_mul_f32_e32 v39, 0x42800000, v39
	v_med3_f32 v35, v35, s24, v150
	v_med3_f32 v39, v39, s24, v150
	v_mul_f32_e32 v43, 0x42800000, v43
	v_mul_f32_e32 v47, 0x42800000, v47
	v_cvt_pk_fp8_f32 v136, v35, v39
	v_med3_f32 v43, v43, s24, v150
	v_med3_f32 v47, v47, s24, v150
	v_cvt_pk_fp8_f32 v136, v43, v47 op_sel:[0,0,1]
	v_mul_f32_e32 v51, 0x42800000, v51
	v_mul_f32_e32 v55, 0x42800000, v55
	v_med3_f32 v51, v51, s24, v150
	v_med3_f32 v55, v55, s24, v150
	v_mul_f32_e32 v59, 0x42800000, v59
	v_mul_f32_e32 v63, 0x42800000, v63
	v_cvt_pk_fp8_f32 v137, v51, v55
	v_med3_f32 v59, v59, s24, v150
	v_med3_f32 v63, v63, s24, v150
	v_cvt_pk_fp8_f32 v137, v59, v63 op_sel:[0,0,1]
	s_nop 0
	ds_write_b128 v147, v[134:137] offset:144
	v_mul_f32_e32 v4, 0x42800000, v4
	v_mul_f32_e32 v8, 0x42800000, v8
	v_med3_f32 v4, v4, s24, v150
	v_med3_f32 v8, v8, s24, v150
	v_mul_f32_e32 v12, 0x42800000, v12
	v_mul_f32_e32 v16, 0x42800000, v16
	v_cvt_pk_fp8_f32 v138, v4, v8
	v_med3_f32 v12, v12, s24, v150
	v_med3_f32 v16, v16, s24, v150
	v_cvt_pk_fp8_f32 v138, v12, v16 op_sel:[0,0,1]
	v_mul_f32_e32 v20, 0x42800000, v20
	v_mul_f32_e32 v24, 0x42800000, v24
	v_med3_f32 v20, v20, s24, v150
	v_med3_f32 v24, v24, s24, v150
	v_mul_f32_e32 v28, 0x42800000, v28
	v_mul_f32_e32 v32, 0x42800000, v32
	v_cvt_pk_fp8_f32 v139, v20, v24
	v_med3_f32 v28, v28, s24, v150
	v_med3_f32 v32, v32, s24, v150
	v_cvt_pk_fp8_f32 v139, v28, v32 op_sel:[0,0,1]
	v_mul_f32_e32 v36, 0x42800000, v36
	v_mul_f32_e32 v40, 0x42800000, v40
	v_med3_f32 v36, v36, s24, v150
	v_med3_f32 v40, v40, s24, v150
	v_mul_f32_e32 v44, 0x42800000, v44
	v_mul_f32_e32 v48, 0x42800000, v48
	v_cvt_pk_fp8_f32 v140, v36, v40
	v_med3_f32 v44, v44, s24, v150
	v_med3_f32 v48, v48, s24, v150
	v_cvt_pk_fp8_f32 v140, v44, v48 op_sel:[0,0,1]
	v_mul_f32_e32 v52, 0x42800000, v52
	v_mul_f32_e32 v56, 0x42800000, v56
	v_med3_f32 v52, v52, s24, v150
	v_med3_f32 v56, v56, s24, v150
	v_mul_f32_e32 v60, 0x42800000, v60
	v_mul_f32_e32 v64, 0x42800000, v64
	v_cvt_pk_fp8_f32 v141, v52, v56
	v_med3_f32 v60, v60, s24, v150
	v_med3_f32 v64, v64, s24, v150
	v_cvt_pk_fp8_f32 v141, v60, v64 op_sel:[0,0,1]
	s_nop 0
	ds_write_b128 v147, v[138:141] offset:288
	v_mul_f32_e32 v5, 0x42800000, v5
	v_mul_f32_e32 v9, 0x42800000, v9
	v_med3_f32 v5, v5, s24, v150
	v_med3_f32 v9, v9, s24, v150
	v_mul_f32_e32 v13, 0x42800000, v13
	v_mul_f32_e32 v17, 0x42800000, v17
	v_cvt_pk_fp8_f32 v142, v5, v9
	v_med3_f32 v13, v13, s24, v150
	v_med3_f32 v17, v17, s24, v150
	v_cvt_pk_fp8_f32 v142, v13, v17 op_sel:[0,0,1]
	v_mul_f32_e32 v21, 0x42800000, v21
	v_mul_f32_e32 v25, 0x42800000, v25
	v_med3_f32 v21, v21, s24, v150
	v_med3_f32 v25, v25, s24, v150
	v_mul_f32_e32 v29, 0x42800000, v29
	v_mul_f32_e32 v33, 0x42800000, v33
	v_cvt_pk_fp8_f32 v143, v21, v25
	v_med3_f32 v29, v29, s24, v150
	v_med3_f32 v33, v33, s24, v150
	v_cvt_pk_fp8_f32 v143, v29, v33 op_sel:[0,0,1]
	v_mul_f32_e32 v37, 0x42800000, v37
	v_mul_f32_e32 v41, 0x42800000, v41
	v_med3_f32 v37, v37, s24, v150
	v_med3_f32 v41, v41, s24, v150
	v_mul_f32_e32 v45, 0x42800000, v45
	v_mul_f32_e32 v49, 0x42800000, v49
	v_cvt_pk_fp8_f32 v144, v37, v41
	v_med3_f32 v45, v45, s24, v150
	v_med3_f32 v49, v49, s24, v150
	v_cvt_pk_fp8_f32 v144, v45, v49 op_sel:[0,0,1]
	v_mul_f32_e32 v53, 0x42800000, v53
	v_mul_f32_e32 v57, 0x42800000, v57
	v_med3_f32 v53, v53, s24, v150
	v_med3_f32 v57, v57, s24, v150
	v_mul_f32_e32 v61, 0x42800000, v61
	v_mul_f32_e32 v65, 0x42800000, v65
	v_cvt_pk_fp8_f32 v145, v53, v57
	v_med3_f32 v61, v61, s24, v150
	v_med3_f32 v65, v65, s24, v150
	v_cvt_pk_fp8_f32 v145, v61, v65 op_sel:[0,0,1]
	s_nop 0
	ds_write_b128 v147, v[142:145] offset:432
	s_waitcnt lgkmcnt(0)
	s_barrier
	ds_read_b128 v[130:133], v148 offset:0
	ds_read_b128 v[134:137], v148 offset:1152
	ds_read_b128 v[138:141], v148 offset:2304
	ds_read_b128 v[142:145], v148 offset:3456
	s_waitcnt lgkmcnt(3)
	global_store_dwordx4 v149, v[130:133], s[14:15] nt
	s_waitcnt lgkmcnt(2)
	global_store_dwordx4 v149, v[134:137], s[14:15] offset:1024 nt
	s_waitcnt lgkmcnt(1)
	global_store_dwordx4 v149, v[138:141], s[14:15] offset:2048 nt
	s_waitcnt lgkmcnt(0)
	global_store_dwordx4 v149, v[142:145], s[14:15] offset:3072 nt
	s_cmp_eq_u32 s25, 0
	s_cbranch_scc1 .Lcq1_done
	s_cmp_eq_u32 s19, 0
	s_cbranch_scc1 .Lcq1_nlA
	s_cmp_lt_u32 s18, 0x2000
	s_cbranch_scc0 .Lcq1_dnLA
	s_lshr_b32 s20, s18, 4
	s_lshl_b32 s20, s20, 21
	s_and_b32 s21, s18, 15
	s_lshl_b32 s21, s21, 10
	s_add_u32 s20, s20, s21
	s_lshl_b32 s21, s93, 18
	s_add_u32 s20, s20, s21
	s_add_u32 s10, s6, s20
	s_addc_u32 s11, s7, 0
	s_movk_i32 s12, 0x4000
	s_lshl_b32 s20, s18, 15
	s_add_u32 s20, s20, 0x30000000
	s_branch .Lcq1_cmLA

; __device__ __forceinline__ void conv8b_run(const Ctx& X, int first, int step, int count) {
;     ...
;         if (j + 1 < count) { cn = conv8b_dec(X, first + (j + 1) * step);
; #pragma unroll
;             for (int i = 0; i < 16; ++i) v[i] = __builtin_nontemporal_load((const f32x4*)(cn.W + (size_t)i * cn.N)); }
.Lcq1_cmLA:
	s_lshl_b32 s21, s93, 12
	s_add_u32 s20, s20, s21
	s_add_u32 s14, s90, s20
	s_addc_u32 s15, s91, 0
	global_load_dwordx4 v[2:5], v146, s[10:11] nt
	s_add_u32 s10, s10, s12
	s_addc_u32 s11, s11, 0
	global_load_dwordx4 v[6:9], v146, s[10:11] nt
	s_add_u32 s10, s10, s12
	s_addc_u32 s11, s11, 0
	global_load_dwordx4 v[10:13], v146, s[10:11] nt
	s_add_u32 s10, s10, s12
	s_addc_u32 s11, s11, 0
	global_load_dwordx4 v[14:17], v146, s[10:11] nt
	s_add_u32 s10, s10, s12
	s_addc_u32 s11, s11, 0
	global_load_dwordx4 v[18:21], v146, s[10:11] nt
	s_add_u32 s10, s10, s12
	s_addc_u32 s11, s11, 0
	global_load_dwordx4 v[22:25], v146, s[10:11] nt
	s_add_u32 s10, s10, s12
	s_addc_u32 s11, s11, 0
	global_load_dwordx4 v[26:29], v146, s[10:11] nt
	s_add_u32 s10, s10, s12
	s_addc_u32 s11, s11, 0
	global_load_dwordx4 v[30:33], v146, s[10:11] nt
	s_add_u32 s10, s10, s12
	s_addc_u32 s11, s11, 0
	global_load_dwordx4 v[34:37], v146, s[10:11] nt
	s_add_u32 s10, s10, s12
	s_addc_u32 s11, s11, 0
	global_load_dwordx4 v[38:41], v146, s[10:11] nt
	s_add_u32 s10, s10, s12
	s_addc_u32 s11, s11, 0
	global_load_dwordx4 v[42:45], v146, s[10:11] nt
	s_add_u32 s10, s10, s12
	s_addc_u32 s11, s11, 0
	global_load_dwordx4 v[46:49], v146, s[10:11] nt
	s_add_u32 s10, s10, s12
	s_addc_u32 s11, s11, 0
	global_load_dwordx4 v[50:53], v146, s[10:11] nt
	s_add_u32 s10, s10, s12
	s_addc_u32 s11, s11, 0
	global_load_dwordx4 v[54:57], v146, s[10:11] nt
	s_add_u32 s10, s10, s12
	s_addc_u32 s11, s11, 0
	global_load_dwordx4 v[58:61], v146, s[10:11] nt
	s_add_u32 s10, s10, s12
	s_addc_u32 s11, s11, 0
	global_load_dwordx4 v[62:65], v146, s[10:11] nt
	s_add_i32 s18, s18, 2
	s_add_i32 s19, s19, -1
	s_branch .Lcq1_nxA
.Lcq1_nlA:
	s_mov_b32 s25, 0

; #define LAS __attribute__((address_space(3)))
; __device__ __forceinline__ void conv8b_run(const Ctx& X, int first, int step, int count) {
;     ...
;         LAS uchar* buf = X.lds + (j & 1) * CVT_BUF;
; #pragma unroll
;         for (int q = 0; q < 4; ++q) { u32x4 o;
;             o.x = pk_fp8x4(v[0][q] * W8_SCALE, v[1][q] * W8_SCALE, v[2][q] * W8_SCALE, v[3][q] * W8_SCALE); o.y = pk_fp8x4(v[4][q] * W8_SCALE, v[5][q] * W8_SCALE, v[6][q] * W8_SCALE, v[7][q] * W8_SCALE);
;             o.z = pk_fp8x4(v[8][q] * W8_SCALE, v[9][q] * W8_SCALE, v[10][q] * W8_SCALE, v[11][q] * W8_SCALE); o.w = pk_fp8x4(v[12][q] * W8_SCALE, v[13][q] * W8_SCALE, v[14][q] * W8_SCALE, v[15][q] * W8_SCALE);
;             *(LAS u32x4*)(buf + (4 * X.lane + q) * CVT_STRIDE + 16 * X.wave) = o; }
;         if (j + 1 < count) { cn = conv8b_dec(X, first + (j + 1) * step);
; #pragma unroll
;             for (int i = 0; i < 16; ++i) v[i] = __builtin_nontemporal_load((const f32x4*)(cn.W + (size_t)i * cn.N)); }
;         asm volatile("s_waitcnt lgkmcnt(0)" ::: "memory"); __builtin_amdgcn_s_barrier();
; #pragma unroll
;         for (int it = 0; it < 4; ++it) { const u32x4 r = *(const LAS u32x4*)(buf + (32 * X.wave + 8 * it + (X.lane >> 3)) * CVT_STRIDE + 16 * (X.lane & 7));
;             __builtin_nontemporal_store(r, (u32x4*)(c.WT + (size_t)it * 8 * 128)); }
.Lcq1_w1B:
	v_mul_f32_e32 v66, 0x42800000, v66
	v_mul_f32_e32 v70, 0x42800000, v70
	v_med3_f32 v66, v66, s24, v150
	v_med3_f32 v70, v70, s24, v150
	v_mul_f32_e32 v74, 0x42800000, v74
	v_mul_f32_e32 v78, 0x42800000, v78
	v_cvt_pk_fp8_f32 v130, v66, v70
	v_med3_f32 v74, v74, s24, v150
	v_med3_f32 v78, v78, s24, v150
	v_cvt_pk_fp8_f32 v130, v74, v78 op_sel:[0,0,1]
	v_mul_f32_e32 v82, 0x42800000, v82
	v_mul_f32_e32 v86, 0x42800000, v86
	v_med3_f32 v82, v82, s24, v150
	v_med3_f32 v86, v86, s24, v150
	v_mul_f32_e32 v90, 0x42800000, v90
	v_mul_f32_e32 v94, 0x42800000, v94
	v_cvt_pk_fp8_f32 v131, v82, v86
	v_med3_f32 v90, v90, s24, v150
	v_med3_f32 v94, v94, s24, v150
	v_cvt_pk_fp8_f32 v131, v90, v94 op_sel:[0,0,1]
	v_mul_f32_e32 v98, 0x42800000, v98
	v_mul_f32_e32 v102, 0x42800000, v102
	v_med3_f32 v98, v98, s24, v150
	v_med3_f32 v102, v102, s24, v150
	v_mul_f32_e32 v106, 0x42800000, v106
	v_mul_f32_e32 v110, 0x42800000, v110
	v_cvt_pk_fp8_f32 v132, v98, v102
	v_med3_f32 v106, v106, s24, v150
	v_med3_f32 v110, v110, s24, v150
	v_cvt_pk_fp8_f32 v132, v106, v110 op_sel:[0,0,1]
	v_mul_f32_e32 v114, 0x42800000, v114
	v_mul_f32_e32 v118, 0x42800000, v118
	v_med3_f32 v114, v114, s24, v150
	v_med3_f32 v118, v118, s24, v150
	v_mul_f32_e32 v122, 0x42800000, v122
	v_mul_f32_e32 v126, 0x42800000, v126
	v_cvt_pk_fp8_f32 v133, v114, v118
	v_med3_f32 v122, v122, s24, v150
	v_med3_f32 v126, v126, s24, v150
	v_cvt_pk_fp8_f32 v133, v122, v126 op_sel:[0,0,1]
	s_nop 0
	ds_write_b128 v147, v[130:133] offset:36864
	v_mul_f32_e32 v67, 0x42800000, v67
	v_mul_f32_e32 v71, 0x42800000, v71
	v_med3_f32 v67, v67, s24, v150
	v_med3_f32 v71, v71, s24, v150
	v_mul_f32_e32 v75, 0x42800000, v75
	v_mul_f32_e32 v79, 0x42800000, v79
	v_cvt_pk_fp8_f32 v134, v67, v71
	v_med3_f32 v75, v75, s24, v150
	v_med3_f32 v79, v79, s24, v150
	v_cvt_pk_fp8_f32 v134, v75, v79 op_sel:[0,0,1]
	v_mul_f32_e32 v83, 0x42800000, v83
	v_mul_f32_e32 v87, 0x42800000, v87
	v_med3_f32 v83, v83, s24, v150
	v_med3_f32 v87, v87, s24, v150
	v_mul_f32_e32 v91, 0x42800000, v91
	v_mul_f32_e32 v95, 0x42800000, v95
	v_cvt_pk_fp8_f32 v135, v83, v87
	v_med3_f32 v91, v91, s24, v150
	v_med3_f32 v95, v95, s24, v150
	v_cvt_pk_fp8_f32 v135, v91, v95 op_sel:[0,0,1]
	v_mul_f32_e32 v99, 0x42800000, v99
	v_mul_f32_e32 v103, 0x42800000, v103
	v_med3_f32 v99, v99, s24, v150
	v_med3_f32 v103, v103, s24, v150
	v_mul_f32_e32 v107, 0x42800000, v107
	v_mul_f32_e32 v111, 0x42800000, v111
	v_cvt_pk_fp8_f32 v136, v99, v103
	v_med3_f32 v107, v107, s24, v150
	v_med3_f32 v111, v111, s24, v150
	v_cvt_pk_fp8_f32 v136, v107, v111 op_sel:[0,0,1]
	v_mul_f32_e32 v115, 0x42800000, v115
	v_mul_f32_e32 v119, 0x42800000, v119
	v_med3_f32 v115, v115, s24, v150
	v_med3_f32 v119, v119, s24, v150
	v_mul_f32_e32 v123, 0x42800000, v123
	v_mul_f32_e32 v127, 0x42800000, v127
	v_cvt_pk_fp8_f32 v137, v115, v119
	v_med3_f32 v123, v123, s24, v150
	v_med3_f32 v127, v127, s24, v150
	v_cvt_pk_fp8_f32 v137, v123, v127 op_sel:[0,0,1]
	s_nop 0
	ds_write_b128 v147, v[134:137] offset:37008
	v_mul_f32_e32 v68, 0x42800000, v68
	v_mul_f32_e32 v72, 0x42800000, v72
	v_med3_f32 v68, v68, s24, v150
	v_med3_f32 v72, v72, s24, v150
	v_mul_f32_e32 v76, 0x42800000, v76
	v_mul_f32_e32 v80, 0x42800000, v80
	v_cvt_pk_fp8_f32 v138, v68, v72
	v_med3_f32 v76, v76, s24, v150
	v_med3_f32 v80, v80, s24, v150
	v_cvt_pk_fp8_f32 v138, v76, v80 op_sel:[0,0,1]
	v_mul_f32_e32 v84, 0x42800000, v84
	v_mul_f32_e32 v88, 0x42800000, v88
	v_med3_f32 v84, v84, s24, v150
	v_med3_f32 v88, v88, s24, v150
	v_mul_f32_e32 v92, 0x42800000, v92
	v_mul_f32_e32 v96, 0x42800000, v96
	v_cvt_pk_fp8_f32 v139, v84, v88
	v_med3_f32 v92, v92, s24, v150
	v_med3_f32 v96, v96, s24, v150
	v_cvt_pk_fp8_f32 v139, v92, v96 op_sel:[0,0,1]
	v_mul_f32_e32 v100, 0x42800000, v100
	v_mul_f32_e32 v104, 0x42800000, v104
	v_med3_f32 v100, v100, s24, v150
	v_med3_f32 v104, v104, s24, v150
	v_mul_f32_e32 v108, 0x42800000, v108
	v_mul_f32_e32 v112, 0x42800000, v112
	v_cvt_pk_fp8_f32 v140, v100, v104
	v_med3_f32 v108, v108, s24, v150
	v_med3_f32 v112, v112, s24, v150
	v_cvt_pk_fp8_f32 v140, v108, v112 op_sel:[0,0,1]
	v_mul_f32_e32 v116, 0x42800000, v116
	v_mul_f32_e32 v120, 0x42800000, v120
	v_med3_f32 v116, v116, s24, v150
	v_med3_f32 v120, v120, s24, v150
	v_mul_f32_e32 v124, 0x42800000, v124
	v_mul_f32_e32 v128, 0x42800000, v128
	v_cvt_pk_fp8_f32 v141, v116, v120
	v_med3_f32 v124, v124, s24, v150
	v_med3_f32 v128, v128, s24, v150
	v_cvt_pk_fp8_f32 v141, v124, v128 op_sel:[0,0,1]
	s_nop 0
	ds_write_b128 v147, v[138:141] offset:37152
	v_mul_f32_e32 v69, 0x42800000, v69
	v_mul_f32_e32 v73, 0x42800000, v73
	v_med3_f32 v69, v69, s24, v150
	v_med3_f32 v73, v73, s24, v150
	v_mul_f32_e32 v77, 0x42800000, v77
	v_mul_f32_e32 v81, 0x42800000, v81
	v_cvt_pk_fp8_f32 v142, v69, v73
	v_med3_f32 v77, v77, s24, v150
	v_med3_f32 v81, v81, s24, v150
	v_cvt_pk_fp8_f32 v142, v77, v81 op_sel:[0,0,1]
	v_mul_f32_e32 v85, 0x42800000, v85
	v_mul_f32_e32 v89, 0x42800000, v89
	v_med3_f32 v85, v85, s24, v150
	v_med3_f32 v89, v89, s24, v150
	v_mul_f32_e32 v93, 0x42800000, v93
	v_mul_f32_e32 v97, 0x42800000, v97
	v_cvt_pk_fp8_f32 v143, v85, v89
	v_med3_f32 v93, v93, s24, v150
	v_med3_f32 v97, v97, s24, v150
	v_cvt_pk_fp8_f32 v143, v93, v97 op_sel:[0,0,1]
	v_mul_f32_e32 v101, 0x42800000, v101
	v_mul_f32_e32 v105, 0x42800000, v105
	v_med3_f32 v101, v101, s24, v150
	v_med3_f32 v105, v105, s24, v150
	v_mul_f32_e32 v109, 0x42800000, v109
	v_mul_f32_e32 v113, 0x42800000, v113
	v_cvt_pk_fp8_f32 v144, v101, v105
	v_med3_f32 v109, v109, s24, v150
	v_med3_f32 v113, v113, s24, v150
	v_cvt_pk_fp8_f32 v144, v109, v113 op_sel:[0,0,1]
	v_mul_f32_e32 v117, 0x42800000, v117
	v_mul_f32_e32 v121, 0x42800000, v121
	v_med3_f32 v117, v117, s24, v150
	v_med3_f32 v121, v121, s24, v150
	v_mul_f32_e32 v125, 0x42800000, v125
	v_mul_f32_e32 v129, 0x42800000, v129
	v_cvt_pk_fp8_f32 v145, v117, v121
	v_med3_f32 v125, v125, s24, v150
	v_med3_f32 v129, v129, s24, v150
	v_cvt_pk_fp8_f32 v145, v125, v129 op_sel:[0,0,1]
	s_nop 0
	ds_write_b128 v147, v[142:145] offset:37296
	s_waitcnt lgkmcnt(0)
	s_barrier
	ds_read_b128 v[130:133], v148 offset:36864
	ds_read_b128 v[134:137], v148 offset:38016
	ds_read_b128 v[138:141], v148 offset:39168
	ds_read_b128 v[142:145], v148 offset:40320
	s_waitcnt lgkmcnt(3)
	global_store_dwordx4 v149, v[130:133], s[16:17] nt
	s_waitcnt lgkmcnt(2)
	global_store_dwordx4 v149, v[134:137], s[16:17] offset:1024 nt
	s_waitcnt lgkmcnt(1)
	global_store_dwordx4 v149, v[138:141], s[16:17] offset:2048 nt
	s_waitcnt lgkmcnt(0)
	global_store_dwordx4 v149, v[142:145], s[16:17] offset:3072 nt
	s_cmp_eq_u32 s25, 0
	s_cbranch_scc1 .Lcq1_done
	s_cmp_eq_u32 s19, 0
	s_cbranch_scc1 .Lcq1_nlB
	s_cmp_lt_u32 s27, 0x2000
	s_cbranch_scc0 .Lcq1_dnLB
	s_lshr_b32 s20, s27, 4
	s_lshl_b32 s20, s20, 21
	s_and_b32 s21, s27, 15
	s_lshl_b32 s21, s21, 10
	s_add_u32 s20, s20, s21
	s_lshl_b32 s21, s93, 18
	s_add_u32 s20, s20, s21
	s_add_u32 s10, s6, s20
	s_addc_u32 s11, s7, 0
	s_movk_i32 s12, 0x4000
	s_lshl_b32 s20, s27, 15
	s_add_u32 s20, s20, 0x30000000
	s_branch .Lcq1_cmLB

; __device__ __forceinline__ void conv8b_run(const Ctx& X, int first, int step, int count) {
;     ...
;         if (j + 1 < count) { cn = conv8b_dec(X, first + (j + 1) * step);
; #pragma unroll
;             for (int i = 0; i < 16; ++i) v[i] = __builtin_nontemporal_load((const f32x4*)(cn.W + (size_t)i * cn.N)); }
.Lcq1_cmLB:
	s_lshl_b32 s21, s93, 12
	s_add_u32 s20, s20, s21
	s_add_u32 s16, s90, s20
	s_addc_u32 s17, s91, 0
	global_load_dwordx4 v[66:69], v146, s[10:11] nt
	s_add_u32 s10, s10, s12
	s_addc_u32 s11, s11, 0
	global_load_dwordx4 v[70:73], v146, s[10:11] nt
	s_add_u32 s10, s10, s12
	s_addc_u32 s11, s11, 0
	global_load_dwordx4 v[74:77], v146, s[10:11] nt
	s_add_u32 s10, s10, s12
	s_addc_u32 s11, s11, 0
	global_load_dwordx4 v[78:81], v146, s[10:11] nt
	s_add_u32 s10, s10, s12
	s_addc_u32 s11, s11, 0
	global_load_dwordx4 v[82:85], v146, s[10:11] nt
	s_add_u32 s10, s10, s12
	s_addc_u32 s11, s11, 0
	global_load_dwordx4 v[86:89], v146, s[10:11] nt
	s_add_u32 s10, s10, s12
	s_addc_u32 s11, s11, 0
	global_load_dwordx4 v[90:93], v146, s[10:11] nt
	s_add_u32 s10, s10, s12
	s_addc_u32 s11, s11, 0
	global_load_dwordx4 v[94:97], v146, s[10:11] nt
	s_add_u32 s10, s10, s12
	s_addc_u32 s11, s11, 0
	global_load_dwordx4 v[98:101], v146, s[10:11] nt
	s_add_u32 s10, s10, s12
	s_addc_u32 s11, s11, 0
	global_load_dwordx4 v[102:105], v146, s[10:11] nt
	s_add_u32 s10, s10, s12
	s_addc_u32 s11, s11, 0
	global_load_dwordx4 v[106:109], v146, s[10:11] nt
	s_add_u32 s10, s10, s12
	s_addc_u32 s11, s11, 0
	global_load_dwordx4 v[110:113], v146, s[10:11] nt
	s_add_u32 s10, s10, s12
	s_addc_u32 s11, s11, 0
	global_load_dwordx4 v[114:117], v146, s[10:11] nt
	s_add_u32 s10, s10, s12
	s_addc_u32 s11, s11, 0
	global_load_dwordx4 v[118:121], v146, s[10:11] nt
	s_add_u32 s10, s10, s12
	s_addc_u32 s11, s11, 0
	global_load_dwordx4 v[122:125], v146, s[10:11] nt
	s_add_u32 s10, s10, s12
	s_addc_u32 s11, s11, 0
	global_load_dwordx4 v[126:129], v146, s[10:11] nt
	s_add_i32 s27, s27, 2
	s_add_i32 s19, s19, -1
	s_branch .Lcq1_nxB

; __device__ __forceinline__ unsigned xb_ld(unsigned* p)              { return __hip_atomic_load(p, __ATOMIC_RELAXED, __HIP_MEMORY_SCOPE_AGENT); }
; __device__ __forceinline__ void xcd_barrier_complete(unsigned* bar, unsigned x, unsigned& nloc, unsigned& nx) {
;     const unsigned G = gridDim.x * gridDim.y * gridDim.z;
;     unsigned sum, cnt, mine, sp = 0u;
;     for (;;) {
;         sum = 0u; cnt = 0u; mine = 0u;
; #pragma unroll
;         for (unsigned j = 0; j < 16; ++j) { const unsigned c = xb_ld(&bar[XB_XCNT(j)]); sum += c; cnt += (c > 0u) ? 1u : 0u; mine = (j == x) ? c : mine; }
; __device__ __forceinline__ void xcd_barrier(const XcdBarrier& b) {
;     asm volatile("s_waitcnt vmcnt(0)" ::: "memory");
;     __syncthreads();
;     if (threadIdx.x == 0) {
;         unsigned* bar = b.bar;
;         __builtin_amdgcn_s_waitcnt(0);
;         unsigned nloc = b.st[0], nx = b.st[1];
;         if (nloc == 0u) { xcd_barrier_complete(bar, b.x, nloc, nx); b.st[0] = nloc; b.st[1] = nx; }
.Lcq1_nxB:
	s_branch .Lcq1_loop
.Lcq1_done:
	s_waitcnt lgkmcnt(0)
	s_barrier
	s_branch .Lcq1_outer
.Lcq1_qdone:
.LBB0_146:
	s_cmp_gt_i32 s95, 2
	s_cselect_b64 s[2:3], -1, 0
	s_and_b64 s[4:5], s[4:5], s[2:3]
	s_andn2_b64 vcc, exec, s[4:5]
	s_cbranch_vccnz .LBB0_196
	s_waitcnt vmcnt(0)
	v_cmp_eq_u32_e32 vcc, 0, v0
	s_waitcnt lgkmcnt(0)
	s_barrier
	s_and_saveexec_b64 s[4:5], vcc
	s_cbranch_execz .LBB0_195
	s_waitcnt vmcnt(7)
	v_mov_b32_e32 v2, s62
	s_waitcnt vmcnt(0) expcnt(0) lgkmcnt(0)
	ds_read_b32 v4, v2
	ds_read_b32 v2, v2 offset:4
	s_waitcnt lgkmcnt(1)
	v_cmp_ne_u32_e32 vcc, 0, v4
	s_cbranch_vccnz .LBB0_163
	v_readlane_b32 s6, v248, 0
	v_readlane_b32 s7, v248, 1
	s_load_dwordx2 s[10:11], s[6:7], 0x4
	s_add_u32 s6, s90, 0x4200
	s_addc_u32 s7, s91, 0
	s_add_u32 s8, s90, 0x4400
	s_addc_u32 s9, s91, 0
	s_waitcnt lgkmcnt(0)
	s_mul_i32 s33, s10, s92
	s_add_u32 s10, s90, 0x4500
	s_mul_i32 s33, s33, s11
	s_addc_u32 s11, s91, 0
	s_add_u32 s12, s90, 0x4600
	s_addc_u32 s13, s91, 0
	s_add_u32 s14, s90, 0x4700
	s_addc_u32 s15, s91, 0
	s_add_u32 s16, s90, 0x4800
	s_addc_u32 s17, s91, 0
	s_add_u32 s18, s90, 0x4900
	s_addc_u32 s19, s91, 0
	s_add_u32 s20, s90, 0x4a00
	s_addc_u32 s21, s91, 0
	s_add_u32 s22, s90, 0x4b00
	s_addc_u32 s23, s91, 0
	s_add_u32 s24, s90, 0x4c00
	s_addc_u32 s25, s91, 0
	s_add_u32 s26, s90, 0x4d00
	s_addc_u32 s27, s91, 0
	s_add_u32 s28, s90, 0x4e00
	s_addc_u32 s29, s91, 0
	s_add_u32 s30, s90, 0x4f00
	s_addc_u32 s31, s91, 0
	s_add_u32 s34, s90, 0x5000
	s_addc_u32 s35, s91, 0
	s_add_u32 s36, s90, 0x5100
	s_addc_u32 s37, s91, 0
	s_add_u32 s38, s90, 0x5200
	s_addc_u32 s39, s91, 0
	s_add_u32 s40, s90, 0x5300
	s_addc_u32 s41, s91, 0
	s_mov_b32 s48, 1
	v_mov_b32_e32 v18, 0
	s_branch .LBB0_151

; #define LAS __attribute__((address_space(3)))
; __device__ __forceinline__ f32x4 mma16(bf16x8 xrow, bf16x8 ycol, f32x4 c) { return __builtin_amdgcn_mfma_f32_16x16x32_bf16(xrow, ycol, c, 0, 0, 0); }
; __device__ __forceinline__ void p4_ret(Ctx& X, int unit) {
;     ...
; #pragma unroll 2
;         for (int ks = 0; ks < 4; ++ks) {
;             const bf16x8 af = *(const LAS bf16x8*)(R1 + l * 544 + (128 * dh + 32 * ks + 8 * fq) * 2);
; #pragma unroll
;             for (int n = 0; n < 16; ++n) { const bf16x8 bf = *(const LAS bf16x8*)(R2 + (16 * n + fr) * 272 + (32 * ks + 8 * fq) * 2); acc[n] = mma16(bf, af, acc[n]); }
;         }
.LBB0_565:
	v_add_u32_e32 v242, s5, v215
	v_add_u32_e32 v141, s5, v214
	v_add_u32_e32 v249, 0x11000, v242
	ds_read_b128 v[114:117], v141
	ds_read_b128 v[238:241], v249
	ds_read_b128 v[244:247], v249 offset:4352
	ds_read_b128 v[250:253], v249 offset:8704
	s_addk_i32 s5, 0x80
	s_cmpk_eq_i32 s5, 0x100
	s_waitcnt lgkmcnt(2)
	v_mfma_f32_16x16x32_bf16 v[74:77], v[238:241], v[114:117], v[74:77]
	ds_read_b128 v[238:241], v249 offset:13056
	s_waitcnt lgkmcnt(2)
	v_mfma_f32_16x16x32_bf16 v[70:73], v[244:247], v[114:117], v[70:73]
	ds_read_b128 v[244:247], v249 offset:17408
	s_waitcnt lgkmcnt(2)
	v_mfma_f32_16x16x32_bf16 v[66:69], v[250:253], v[114:117], v[66:69]
	ds_read_b128 v[250:253], v249 offset:21760
	s_waitcnt lgkmcnt(2)
	v_mfma_f32_16x16x32_bf16 v[62:65], v[238:241], v[114:117], v[62:65]
	ds_read_b128 v[238:241], v249 offset:26112
	s_waitcnt lgkmcnt(2)
	v_mfma_f32_16x16x32_bf16 v[58:61], v[244:247], v[114:117], v[58:61]
	ds_read_b128 v[244:247], v249 offset:30464
	s_waitcnt lgkmcnt(2)
	v_mfma_f32_16x16x32_bf16 v[54:57], v[250:253], v[114:117], v[54:57]
	ds_read_b128 v[250:253], v249 offset:34816
	s_waitcnt lgkmcnt(2)
	v_mfma_f32_16x16x32_bf16 v[50:53], v[238:241], v[114:117], v[50:53]
	ds_read_b128 v[238:241], v249 offset:39168
	s_waitcnt lgkmcnt(2)
	v_mfma_f32_16x16x32_bf16 v[46:49], v[244:247], v[114:117], v[46:49]
	ds_read_b128 v[244:247], v249 offset:43520
	s_waitcnt lgkmcnt(2)
	v_mfma_f32_16x16x32_bf16 v[42:45], v[250:253], v[114:117], v[42:45]
	ds_read_b128 v[250:253], v249 offset:47872
	s_waitcnt lgkmcnt(2)
	v_mfma_f32_16x16x32_bf16 v[38:41], v[238:241], v[114:117], v[38:41]
	ds_read_b128 v[238:241], v249 offset:52224
	s_waitcnt lgkmcnt(2)
	v_mfma_f32_16x16x32_bf16 v[34:37], v[244:247], v[114:117], v[34:37]
	ds_read_b128 v[244:247], v249 offset:56576
	s_waitcnt lgkmcnt(2)
	v_mfma_f32_16x16x32_bf16 v[30:33], v[250:253], v[114:117], v[30:33]
	ds_read_b128 v[250:253], v249 offset:60928
	s_waitcnt lgkmcnt(2)
	v_mfma_f32_16x16x32_bf16 v[26:29], v[238:241], v[114:117], v[26:29]
	ds_read_b128 v[238:241], v249 offset:65280
	s_waitcnt lgkmcnt(2)
	v_mfma_f32_16x16x32_bf16 v[18:21], v[244:247], v[114:117], v[18:21]
	ds_read_b128 v[244:247], v249 offset:64
	s_waitcnt lgkmcnt(2)
	v_mfma_f32_16x16x32_bf16 v[10:13], v[250:253], v[114:117], v[10:13]
	ds_read_b128 v[250:253], v249 offset:4416
	s_waitcnt lgkmcnt(2)
	v_mfma_f32_16x16x32_bf16 v[78:81], v[238:241], v[114:117], v[78:81]
	ds_read_b128 v[238:241], v249 offset:8768
	ds_read_b128 v[114:117], v141 offset:64
	s_waitcnt lgkmcnt(0)
	v_mfma_f32_16x16x32_bf16 v[74:77], v[244:247], v[114:117], v[74:77]
	ds_read_b128 v[244:247], v249 offset:13120
	s_waitcnt lgkmcnt(2)
	v_mfma_f32_16x16x32_bf16 v[70:73], v[250:253], v[114:117], v[70:73]
	ds_read_b128 v[250:253], v249 offset:17472
	s_waitcnt lgkmcnt(2)
	v_mfma_f32_16x16x32_bf16 v[66:69], v[238:241], v[114:117], v[66:69]
	ds_read_b128 v[238:241], v249 offset:21824
	s_waitcnt lgkmcnt(2)
	v_mfma_f32_16x16x32_bf16 v[62:65], v[244:247], v[114:117], v[62:65]
	ds_read_b128 v[244:247], v249 offset:26176
	s_waitcnt lgkmcnt(2)
	v_mfma_f32_16x16x32_bf16 v[58:61], v[250:253], v[114:117], v[58:61]
	ds_read_b128 v[250:253], v249 offset:30528
	s_waitcnt lgkmcnt(2)
	v_mfma_f32_16x16x32_bf16 v[54:57], v[238:241], v[114:117], v[54:57]
	ds_read_b128 v[238:241], v249 offset:34880
	s_waitcnt lgkmcnt(2)
	v_mfma_f32_16x16x32_bf16 v[50:53], v[244:247], v[114:117], v[50:53]
	ds_read_b128 v[244:247], v249 offset:39232
	s_waitcnt lgkmcnt(2)
	v_mfma_f32_16x16x32_bf16 v[46:49], v[250:253], v[114:117], v[46:49]
	ds_read_b128 v[250:253], v249 offset:43584
	s_waitcnt lgkmcnt(2)
	v_mfma_f32_16x16x32_bf16 v[42:45], v[238:241], v[114:117], v[42:45]
	ds_read_b128 v[238:241], v249 offset:47936
	s_waitcnt lgkmcnt(2)
	v_mfma_f32_16x16x32_bf16 v[38:41], v[244:247], v[114:117], v[38:41]
	ds_read_b128 v[244:247], v249 offset:52288
	s_waitcnt lgkmcnt(2)
	v_mfma_f32_16x16x32_bf16 v[34:37], v[250:253], v[114:117], v[34:37]
	ds_read_b128 v[250:253], v249 offset:56640
	s_waitcnt lgkmcnt(2)
	v_mfma_f32_16x16x32_bf16 v[30:33], v[238:241], v[114:117], v[30:33]
	ds_read_b128 v[238:241], v249 offset:60992
	s_waitcnt lgkmcnt(2)
	v_mfma_f32_16x16x32_bf16 v[26:29], v[244:247], v[114:117], v[26:29]
	ds_read_b128 v[244:247], v249 offset:65344
	s_waitcnt lgkmcnt(2)
	v_mfma_f32_16x16x32_bf16 v[18:21], v[250:253], v[114:117], v[18:21]
	s_waitcnt lgkmcnt(1)
	v_mfma_f32_16x16x32_bf16 v[10:13], v[238:241], v[114:117], v[10:13]
	s_waitcnt lgkmcnt(0)
	v_mfma_f32_16x16x32_bf16 v[78:81], v[244:247], v[114:117], v[78:81]
	s_cbranch_scc0 .LBB0_565
	s_load_dwordx4 s[76:79], s[0:1], 0x98
	s_lshl_b32 s5, s12, 1
	v_mov_b32_e32 v141, v119
	s_waitcnt lgkmcnt(0)
	s_barrier
	s_add_u32 s74, s78, s5
	s_addc_u32 s75, s79, 0
	s_waitcnt vmcnt(7)
	ds_write_b128 v222, v[82:85]
	s_waitcnt vmcnt(6)
	ds_write_b128 v223, v[86:89]
	s_waitcnt vmcnt(5)
	ds_write_b128 v224, v[90:93]
	s_waitcnt vmcnt(4)
	ds_write_b128 v225, v[94:97]
	s_waitcnt vmcnt(3)
	ds_write_b128 v226, v[98:101]
	s_waitcnt vmcnt(2)
	ds_write_b128 v227, v[102:105]
	s_waitcnt vmcnt(1)
	ds_write_b128 v228, v[106:109]
	s_waitcnt vmcnt(0)
	ds_write_b128 v229, v[110:113]
	v_lshl_add_u64 v[82:83], s[74:75], 0, v[140:141]
	s_mov_b64 s[6:7], 0x16000000
	v_lshl_add_u64 v[106:107], v[82:83], 0, s[6:7]
	v_lshl_add_u64 v[82:83], v[106:107], 0, v[142:143]
	v_lshl_add_u64 v[86:87], v[106:107], 0, v[144:145]
	v_lshl_add_u64 v[90:91], v[106:107], 0, v[146:147]
	v_lshl_add_u64 v[94:95], v[106:107], 0, v[148:149]
	v_lshl_add_u64 v[98:99], v[106:107], 0, v[150:151]
	v_lshl_add_u64 v[102:103], v[106:107], 0, v[152:153]
	v_lshl_add_u64 v[108:109], v[106:107], 0, v[154:155]
	v_lshl_add_u64 v[110:111], v[106:107], 0, v[156:157]
	s_waitcnt lgkmcnt(0)
	s_barrier
	global_load_dwordx4 v[82:85], v[82:83], off nt
	s_nop 0
	global_load_dwordx4 v[86:89], v[86:87], off nt
	s_nop 0
	global_load_dwordx4 v[90:93], v[90:91], off nt
	s_nop 0
	global_load_dwordx4 v[94:97], v[94:95], off nt
	s_nop 0
	global_load_dwordx4 v[98:101], v[98:99], off nt
	s_nop 0
	global_load_dwordx4 v[102:105], v[102:103], off nt
	s_nop 0
	global_load_dwordx4 v[106:109], v[108:109], off nt
	s_nop 0
	global_load_dwordx4 v[110:113], v[110:111], off nt
	s_mov_b32 s6, 0
; #define LAS __attribute__((address_space(3)))
; __device__ __forceinline__ f32x4 mma16(bf16x8 xrow, bf16x8 ycol, f32x4 c) { return __builtin_amdgcn_mfma_f32_16x16x32_bf16(xrow, ycol, c, 0, 0, 0); }
; __device__ __forceinline__ void p4_ret(Ctx& X, int unit) {
;     ...
; #pragma unroll 2
;         for (int ks = 0; ks < 4; ++ks) {
;             const bf16x8 af = *(const LAS bf16x8*)(R1 + l * 544 + (128 * dh + 32 * ks + 8 * fq) * 2);
; #pragma unroll
;             for (int n = 0; n < 16; ++n) { const bf16x8 bf = *(const LAS bf16x8*)(R2 + (16 * n + fr) * 272 + (32 * ks + 8 * fq) * 2); acc[n] = mma16(bf, af, acc[n]); }
;         }
;         __syncthreads();
;     }
;     { const float qd = exp2f(lg * (float)(l + 1));
; #pragma unroll
;       for (int n = 0; n < 16; ++n) acc[n] = acc[n] * qd; }
; #pragma unroll
;     for (int i = 0; i < 8; ++i) { const int q = tid + 512 * i, s_ = q >> 5, vc = q & 31; *(LAS u32x4*)(R2 + s_ * 544 + vc * 16) = P[i]; }
;     __syncthreads();
.LBB0_567:
	v_add_u32_e32 v146, s6, v217
	v_add_u32_e32 v141, s6, v216
	v_add_u32_e32 v249, 0x11000, v146
	ds_read_b128 v[114:117], v141
	ds_read_b128 v[142:145], v249
	ds_read_b128 v[244:247], v249 offset:4352
	ds_read_b128 v[250:253], v249 offset:8704
	s_addk_i32 s6, 0x80
	s_cmpk_lg_i32 s6, 0x100
	s_waitcnt lgkmcnt(2)
	v_mfma_f32_16x16x32_bf16 v[74:77], v[142:145], v[114:117], v[74:77]
	ds_read_b128 v[142:145], v249 offset:13056
	s_waitcnt lgkmcnt(2)
	v_mfma_f32_16x16x32_bf16 v[70:73], v[244:247], v[114:117], v[70:73]
	ds_read_b128 v[244:247], v249 offset:17408
	s_waitcnt lgkmcnt(2)
	v_mfma_f32_16x16x32_bf16 v[66:69], v[250:253], v[114:117], v[66:69]
	ds_read_b128 v[250:253], v249 offset:21760
	s_waitcnt lgkmcnt(2)
	v_mfma_f32_16x16x32_bf16 v[62:65], v[142:145], v[114:117], v[62:65]
	ds_read_b128 v[142:145], v249 offset:26112
	s_waitcnt lgkmcnt(2)
	v_mfma_f32_16x16x32_bf16 v[58:61], v[244:247], v[114:117], v[58:61]
	ds_read_b128 v[244:247], v249 offset:30464
	s_waitcnt lgkmcnt(2)
	v_mfma_f32_16x16x32_bf16 v[54:57], v[250:253], v[114:117], v[54:57]
	ds_read_b128 v[250:253], v249 offset:34816
	s_waitcnt lgkmcnt(2)
	v_mfma_f32_16x16x32_bf16 v[50:53], v[142:145], v[114:117], v[50:53]
	ds_read_b128 v[142:145], v249 offset:39168
	s_waitcnt lgkmcnt(2)
	v_mfma_f32_16x16x32_bf16 v[46:49], v[244:247], v[114:117], v[46:49]
	ds_read_b128 v[244:247], v249 offset:43520
	s_waitcnt lgkmcnt(2)
	v_mfma_f32_16x16x32_bf16 v[42:45], v[250:253], v[114:117], v[42:45]
	ds_read_b128 v[250:253], v249 offset:47872
	s_waitcnt lgkmcnt(2)
	v_mfma_f32_16x16x32_bf16 v[38:41], v[142:145], v[114:117], v[38:41]
	ds_read_b128 v[142:145], v249 offset:52224
	s_waitcnt lgkmcnt(2)
	v_mfma_f32_16x16x32_bf16 v[34:37], v[244:247], v[114:117], v[34:37]
	ds_read_b128 v[244:247], v249 offset:56576
	s_waitcnt lgkmcnt(2)
	v_mfma_f32_16x16x32_bf16 v[30:33], v[250:253], v[114:117], v[30:33]
	ds_read_b128 v[250:253], v249 offset:60928
	s_waitcnt lgkmcnt(2)
	v_mfma_f32_16x16x32_bf16 v[26:29], v[142:145], v[114:117], v[26:29]
	ds_read_b128 v[142:145], v249 offset:65280
	s_waitcnt lgkmcnt(2)
	v_mfma_f32_16x16x32_bf16 v[18:21], v[244:247], v[114:117], v[18:21]
	ds_read_b128 v[244:247], v249 offset:64
	s_waitcnt lgkmcnt(2)
	v_mfma_f32_16x16x32_bf16 v[10:13], v[250:253], v[114:117], v[10:13]
	ds_read_b128 v[250:253], v249 offset:4416
	s_waitcnt lgkmcnt(2)
	v_mfma_f32_16x16x32_bf16 v[78:81], v[142:145], v[114:117], v[78:81]
	ds_read_b128 v[142:145], v249 offset:8768
	ds_read_b128 v[114:117], v141 offset:64
	s_waitcnt lgkmcnt(0)
	v_mfma_f32_16x16x32_bf16 v[74:77], v[244:247], v[114:117], v[74:77]
	ds_read_b128 v[244:247], v249 offset:13120
	s_waitcnt lgkmcnt(2)
	v_mfma_f32_16x16x32_bf16 v[70:73], v[250:253], v[114:117], v[70:73]
	ds_read_b128 v[250:253], v249 offset:17472
	s_waitcnt lgkmcnt(2)
	v_mfma_f32_16x16x32_bf16 v[66:69], v[142:145], v[114:117], v[66:69]
	ds_read_b128 v[142:145], v249 offset:21824
	s_waitcnt lgkmcnt(2)
	v_mfma_f32_16x16x32_bf16 v[62:65], v[244:247], v[114:117], v[62:65]
	ds_read_b128 v[244:247], v249 offset:26176
	s_waitcnt lgkmcnt(2)
	v_mfma_f32_16x16x32_bf16 v[58:61], v[250:253], v[114:117], v[58:61]
	ds_read_b128 v[250:253], v249 offset:30528
	s_waitcnt lgkmcnt(2)
	v_mfma_f32_16x16x32_bf16 v[54:57], v[142:145], v[114:117], v[54:57]
	ds_read_b128 v[142:145], v249 offset:34880
	s_waitcnt lgkmcnt(2)
	v_mfma_f32_16x16x32_bf16 v[50:53], v[244:247], v[114:117], v[50:53]
	ds_read_b128 v[244:247], v249 offset:39232
	s_waitcnt lgkmcnt(2)
	v_mfma_f32_16x16x32_bf16 v[46:49], v[250:253], v[114:117], v[46:49]
	ds_read_b128 v[250:253], v249 offset:43584
	s_waitcnt lgkmcnt(2)
	v_mfma_f32_16x16x32_bf16 v[42:45], v[142:145], v[114:117], v[42:45]
	ds_read_b128 v[142:145], v249 offset:47936
	s_waitcnt lgkmcnt(2)
	v_mfma_f32_16x16x32_bf16 v[38:41], v[244:247], v[114:117], v[38:41]
	ds_read_b128 v[244:247], v249 offset:52288
	s_waitcnt lgkmcnt(2)
	v_mfma_f32_16x16x32_bf16 v[34:37], v[250:253], v[114:117], v[34:37]
	ds_read_b128 v[250:253], v249 offset:56640
	s_waitcnt lgkmcnt(2)
	v_mfma_f32_16x16x32_bf16 v[30:33], v[142:145], v[114:117], v[30:33]
	ds_read_b128 v[142:145], v249 offset:60992
	s_waitcnt lgkmcnt(2)
	v_mfma_f32_16x16x32_bf16 v[26:29], v[244:247], v[114:117], v[26:29]
	ds_read_b128 v[244:247], v249 offset:65344
	s_waitcnt lgkmcnt(2)
	v_mfma_f32_16x16x32_bf16 v[18:21], v[250:253], v[114:117], v[18:21]
	s_waitcnt lgkmcnt(1)
	v_mfma_f32_16x16x32_bf16 v[10:13], v[142:145], v[114:117], v[10:13]
	s_waitcnt lgkmcnt(0)
	v_mfma_f32_16x16x32_bf16 v[78:81], v[244:247], v[114:117], v[78:81]
	s_cbranch_scc1 .LBB0_567
	v_mul_f32_e32 v114, s2, v211
	v_cmp_gt_f32_e32 vcc, s10, v114
	s_barrier
	s_nop 0
	v_cndmask_b32_e32 v115, 0, v221, vcc
	v_fmac_f32_e32 v115, s2, v211
	v_exp_f32_e32 v115, v115
	s_waitcnt vmcnt(7)
	ds_write_b128 v230, v[82:85]
	s_waitcnt vmcnt(6)
	ds_write_b128 v231, v[86:89]
	s_waitcnt vmcnt(5)
	ds_write_b128 v232, v[90:93]
	s_waitcnt vmcnt(4)
	ds_write_b128 v233, v[94:97]
	s_waitcnt vmcnt(3)
	ds_write_b128 v234, v[98:101]
	s_waitcnt vmcnt(2)
	ds_write_b128 v235, v[102:105]
	s_waitcnt vmcnt(1)
	ds_write_b128 v236, v[106:109]
	s_waitcnt vmcnt(0)
	ds_write_b128 v237, v[110:113]
	s_waitcnt lgkmcnt(0)
	s_barrier
; #define LAS __attribute__((address_space(3)))
; #define PROJ_AT(X, row, col) (XP_PROJ(X) + (size_t)((col) >> 8) * PANP + (size_t)(row) * 256 + ((col) & 255))
; __device__ __forceinline__ f32x4 mma16(bf16x8 xrow, bf16x8 ycol, f32x4 c) { return __builtin_amdgcn_mfma_f32_16x16x32_bf16(xrow, ycol, c, 0, 0, 0); }
; __device__ __forceinline__ void p4_ret(Ctx& X, int unit) {
;     ...
;     { const float qd = exp2f(lg * (float)(l + 1));
; #pragma unroll
;       for (int n = 0; n < 16; ++n) acc[n] = acc[n] * qd; }
; #pragma unroll
;     for (int i = 0; i < 8; ++i) { const int q = tid + 512 * i, s_ = q >> 5, vc = q & 31; *(LAS u32x4*)(R2 + s_ * 544 + vc * 16) = P[i]; }
;     __syncthreads();
;     const bf16* gp = PROJ_AT(X, t0 + l, C_G + h * 256) + 4 * fq; bf16* op = XP_MIX(X) + (size_t)(4 * h) * PANE_A + (size_t)(t0 + l) * 64 + 4 * fq;
;     u32x2 gv[16];
; #pragma unroll
;     for (int n = 0; n < 16; ++n) gv[n] = __builtin_nontemporal_load((const u32x2*)(gp + 16 * n));
;     const int trp = (4 * fq + q4) * 544 + 8 * p4;
; #pragma unroll
;     for (int k2 = 0; k2 < 4; ++k2) if (2 * k2 <= w) {
; #pragma unroll
;         for (int n = 0; n < 16; ++n) { const bf16x8 bf = tr_frag(R2 + (32 * k2) * 544 + (16 * n) * 2 + trp, 16 * 544); acc[n] = mma16(bf, scf[k2], acc[n]); }
	ds_read_b64_tr_b16 v[84:85], v212 offset:8704
	ds_read_b64_tr_b16 v[82:83], v212
	v_cndmask_b32_e32 v114, 0, v220, vcc
	v_ldexp_f32 v116, v115, v114
	v_pk_mul_f32 v[76:77], v[116:117], v[76:77] op_sel_hi:[0,1]
	v_pk_mul_f32 v[74:75], v[116:117], v[74:75] op_sel_hi:[0,1]
	ds_read_b64_tr_b16 v[88:89], v212 offset:8736
	ds_read_b64_tr_b16 v[86:87], v212 offset:32
	ds_read_b64_tr_b16 v[90:91], v212 offset:64
	ds_read_b64_tr_b16 v[94:95], v212 offset:96
	ds_read_b64_tr_b16 v[92:93], v212 offset:8768
	ds_read_b64_tr_b16 v[96:97], v212 offset:8800
	s_waitcnt lgkmcnt(6)
	v_mfma_f32_16x16x32_bf16 v[74:77], v[82:85], v[2:5], v[74:77]
	ds_read_b64_tr_b16 v[82:83], v212 offset:128
	ds_read_b64_tr_b16 v[84:85], v212 offset:8832
	v_pk_mul_f32 v[72:73], v[116:117], v[72:73] op_sel_hi:[0,1]
	v_pk_mul_f32 v[70:71], v[116:117], v[70:71] op_sel_hi:[0,1]
	v_pk_mul_f32 v[68:69], v[116:117], v[68:69] op_sel_hi:[0,1]
	v_pk_mul_f32 v[66:67], v[116:117], v[66:67] op_sel_hi:[0,1]
	v_pk_mul_f32 v[64:65], v[116:117], v[64:65] op_sel_hi:[0,1]
	v_pk_mul_f32 v[62:63], v[116:117], v[62:63] op_sel_hi:[0,1]
	v_pk_mul_f32 v[60:61], v[116:117], v[60:61] op_sel_hi:[0,1]
	v_pk_mul_f32 v[58:59], v[116:117], v[58:59] op_sel_hi:[0,1]
	s_waitcnt lgkmcnt(6)
	v_mfma_f32_16x16x32_bf16 v[70:73], v[86:89], v[2:5], v[70:73]
	v_add_u32_e32 v114, s11, v177
	v_ashrrev_i32_e32 v115, 31, v114
	v_pk_mul_f32 v[44:45], v[116:117], v[44:45] op_sel_hi:[0,1]
	s_waitcnt lgkmcnt(3)
	v_mfma_f32_16x16x32_bf16 v[66:69], v[90:93], v[2:5], v[66:69]
	v_mul_f32_e64 v42, v116, v42
	v_mul_f32_e64 v43, v116, v43
	v_lshlrev_b64 v[98:99], 9, v[114:115]
	s_mov_b32 s2, 0x17000000
	s_waitcnt lgkmcnt(2)
	v_mfma_f32_16x16x32_bf16 v[62:65], v[94:97], v[2:5], v[62:65]
	ds_read_b64_tr_b16 v[88:89], v212 offset:8864
	ds_read_b64_tr_b16 v[86:87], v212 offset:160
	ds_read_b64_tr_b16 v[90:91], v212 offset:192
	ds_read_b64_tr_b16 v[94:95], v212 offset:224
	ds_read_b64_tr_b16 v[92:93], v212 offset:8896
	ds_read_b64_tr_b16 v[96:97], v212 offset:8928
	v_pk_mul_f32 v[56:57], v[116:117], v[56:57] op_sel_hi:[0,1]
	v_pk_mul_f32 v[54:55], v[116:117], v[54:55] op_sel_hi:[0,1]
	s_waitcnt lgkmcnt(6)
	v_mfma_f32_16x16x32_bf16 v[58:61], v[82:85], v[2:5], v[58:61]
	ds_read_b64_tr_b16 v[82:83], v212 offset:256
	ds_read_b64_tr_b16 v[84:85], v212 offset:8960
	v_pk_mul_f32 v[52:53], v[116:117], v[52:53] op_sel_hi:[0,1]
	v_pk_mul_f32 v[50:51], v[116:117], v[50:51] op_sel_hi:[0,1]
	s_waitcnt lgkmcnt(0)
	v_mfma_f32_16x16x32_bf16 v[42:45], v[82:85], v[2:5], v[42:45]
	v_lshl_add_u64 v[82:83], s[74:75], 0, v[98:99]
	v_lshl_add_u64 v[82:83], v[82:83], 0, v[118:119]
	v_pk_mul_f32 v[48:49], v[116:117], v[48:49] op_sel_hi:[0,1]
	v_pk_mul_f32 v[46:47], v[116:117], v[46:47] op_sel_hi:[0,1]
	s_mov_b64 s[6:7], 0x17000000
	v_add_co_u32_e32 v112, vcc, s2, v82
	v_mfma_f32_16x16x32_bf16 v[54:57], v[86:89], v[2:5], v[54:57]
	v_lshl_add_u64 v[150:151], v[82:83], 0, s[6:7]
	v_addc_co_u32_e32 v113, vcc, 0, v83, vcc
	v_mfma_f32_16x16x32_bf16 v[50:53], v[90:93], v[2:5], v[50:53]
	v_mul_f32_e64 v40, v116, v40
	v_mul_f32_e64 v41, v116, v41
	v_pk_mul_f32 v[38:39], v[116:117], v[38:39] op_sel_hi:[0,1]
	v_pk_mul_f32 v[36:37], v[116:117], v[36:37] op_sel_hi:[0,1]
	v_mfma_f32_16x16x32_bf16 v[46:49], v[94:97], v[2:5], v[46:49]
	ds_read_b64_tr_b16 v[88:89], v212 offset:8992
	ds_read_b64_tr_b16 v[86:87], v212 offset:288
	ds_read_b64_tr_b16 v[90:91], v212 offset:320
	ds_read_b64_tr_b16 v[94:95], v212 offset:352
	ds_read_b64_tr_b16 v[92:93], v212 offset:9024
	ds_read_b64_tr_b16 v[96:97], v212 offset:9056
	ds_read_b64_tr_b16 v[82:83], v212 offset:384
	ds_read_b64_tr_b16 v[84:85], v212 offset:9088
	v_pk_mul_f32 v[34:35], v[116:117], v[34:35] op_sel_hi:[0,1]
	v_pk_mul_f32 v[32:33], v[116:117], v[32:33] op_sel_hi:[0,1]
	v_pk_mul_f32 v[30:31], v[116:117], v[30:31] op_sel_hi:[0,1]
	v_pk_mul_f32 v[28:29], v[116:117], v[28:29] op_sel_hi:[0,1]
	v_pk_mul_f32 v[26:27], v[116:117], v[26:27] op_sel_hi:[0,1]
	v_pk_mul_f32 v[20:21], v[116:117], v[20:21] op_sel_hi:[0,1]
	v_pk_mul_f32 v[18:19], v[116:117], v[18:19] op_sel_hi:[0,1]
	s_waitcnt lgkmcnt(6)
	v_mfma_f32_16x16x32_bf16 v[38:41], v[86:89], v[2:5], v[38:41]
	global_load_dwordx2 v[110:111], v[150:151], off offset:32 nt
	global_load_dwordx2 v[108:109], v[150:151], off offset:64 nt
	global_load_dwordx2 v[106:107], v[150:151], off offset:96 nt
	global_load_dwordx2 v[104:105], v[150:151], off offset:128 nt
	ds_read_b64_tr_b16 v[88:89], v212 offset:9120
	ds_read_b64_tr_b16 v[86:87], v212 offset:416
	ds_read_b64_tr_b16 v[142:143], v212 offset:448
	ds_read_b64_tr_b16 v[146:147], v212 offset:480
	ds_read_b64_tr_b16 v[144:145], v212 offset:9152
	ds_read_b64_tr_b16 v[148:149], v212 offset:9184
	v_pk_mul_f32 v[12:13], v[116:117], v[12:13] op_sel_hi:[0,1]
	s_waitcnt lgkmcnt(9)
	v_mfma_f32_16x16x32_bf16 v[34:37], v[90:93], v[2:5], v[34:37]
	v_mul_f32_e64 v10, v116, v10
	v_mul_f32_e64 v11, v116, v11
	v_pk_mul_f32 v[80:81], v[116:117], v[80:81] op_sel_hi:[0,1]
	v_pk_mul_f32 v[78:79], v[116:117], v[78:79] op_sel_hi:[0,1]
	s_waitcnt lgkmcnt(8)
	v_mfma_f32_16x16x32_bf16 v[30:33], v[94:97], v[2:5], v[30:33]
	global_load_dwordx2 v[102:103], v[150:151], off offset:160 nt
	global_load_dwordx2 v[100:101], v[150:151], off offset:192 nt
	global_load_dwordx2 v[98:99], v[150:151], off offset:224 nt
	global_load_dwordx2 v[96:97], v[150:151], off offset:256 nt
	s_and_b64 vcc, exec, s[86:87]
	s_waitcnt lgkmcnt(6)
	v_mfma_f32_16x16x32_bf16 v[26:29], v[82:85], v[2:5], v[26:29]
	s_waitcnt lgkmcnt(4)
	v_mfma_f32_16x16x32_bf16 v[18:21], v[86:89], v[2:5], v[18:21]
	global_load_dwordx2 v[94:95], v[150:151], off offset:288 nt
	global_load_dwordx2 v[92:93], v[150:151], off offset:320 nt
	global_load_dwordx2 v[90:91], v[150:151], off offset:352 nt
	global_load_dwordx2 v[88:89], v[150:151], off offset:384 nt
	s_nop 0
	global_load_dwordx2 v[112:113], v[112:113], off nt
	s_nop 0
	global_load_dwordx2 v[86:87], v[150:151], off offset:416 nt
	global_load_dwordx2 v[84:85], v[150:151], off offset:448 nt
	global_load_dwordx2 v[82:83], v[150:151], off offset:480 nt
	s_waitcnt lgkmcnt(1)
	v_mfma_f32_16x16x32_bf16 v[10:13], v[142:145], v[2:5], v[10:13]
	s_waitcnt lgkmcnt(0)
	v_mfma_f32_16x16x32_bf16 v[2:5], v[146:149], v[2:5], v[78:81]
	s_cbranch_vccnz .LBB0_571
	s_and_b64 vcc, exec, s[72:73]
	s_cbranch_vccz .LBB0_572

; __device__ __forceinline__ f32x4 mma16(bf16x8 xrow, bf16x8 ycol, f32x4 c) { return __builtin_amdgcn_mfma_f32_16x16x32_bf16(xrow, ycol, c, 0, 0, 0); }
; __device__ __forceinline__ void p4_ret(Ctx& X, int unit) {
;     ...
; #pragma unroll
;     for (int k2 = 0; k2 < 4; ++k2) if (2 * k2 <= w) {
; #pragma unroll
;         for (int n = 0; n < 16; ++n) { const bf16x8 bf = tr_frag(R2 + (32 * k2) * 544 + (16 * n) * 2 + trp, 16 * 544); acc[n] = mma16(bf, scf[k2], acc[n]); }
;     }
.LBB0_571:
	s_nop 1
	ds_read_b64_tr_b16 v[142:143], v212 offset:17408
	ds_read_b64_tr_b16 v[144:145], v212 offset:26112
	ds_read_b64_tr_b16 v[244:245], v212 offset:17440
	ds_read_b64_tr_b16 v[246:247], v212 offset:26144
	ds_read_b64_tr_b16 v[250:251], v212 offset:17472
	ds_read_b64_tr_b16 v[252:253], v212 offset:26176
	ds_read_b64_tr_b16 v[78:79], v212 offset:17504
	ds_read_b64_tr_b16 v[80:81], v212 offset:26208
	s_waitcnt lgkmcnt(6)
	v_mfma_f32_16x16x32_bf16 v[74:77], v[142:145], v[22:25], v[74:77]
	ds_read_b64_tr_b16 v[142:143], v212 offset:17536
	ds_read_b64_tr_b16 v[144:145], v212 offset:26240
	s_waitcnt lgkmcnt(6)
	v_mfma_f32_16x16x32_bf16 v[70:73], v[244:247], v[22:25], v[70:73]
	ds_read_b64_tr_b16 v[244:245], v212 offset:17568
	ds_read_b64_tr_b16 v[246:247], v212 offset:26272
	s_waitcnt lgkmcnt(6)
	v_mfma_f32_16x16x32_bf16 v[66:69], v[250:253], v[22:25], v[66:69]
	ds_read_b64_tr_b16 v[250:251], v212 offset:17600
	ds_read_b64_tr_b16 v[252:253], v212 offset:26304
	s_waitcnt lgkmcnt(6)
	v_mfma_f32_16x16x32_bf16 v[62:65], v[78:81], v[22:25], v[62:65]
	ds_read_b64_tr_b16 v[78:79], v212 offset:17632
	ds_read_b64_tr_b16 v[80:81], v212 offset:26336
	s_waitcnt lgkmcnt(6)
	v_mfma_f32_16x16x32_bf16 v[58:61], v[142:145], v[22:25], v[58:61]
	ds_read_b64_tr_b16 v[142:143], v212 offset:17664
	ds_read_b64_tr_b16 v[144:145], v212 offset:26368
	s_waitcnt lgkmcnt(6)
	v_mfma_f32_16x16x32_bf16 v[54:57], v[244:247], v[22:25], v[54:57]
	ds_read_b64_tr_b16 v[244:245], v212 offset:17696
	ds_read_b64_tr_b16 v[246:247], v212 offset:26400
	s_waitcnt lgkmcnt(6)
	v_mfma_f32_16x16x32_bf16 v[50:53], v[250:253], v[22:25], v[50:53]
	ds_read_b64_tr_b16 v[250:251], v212 offset:17728
	ds_read_b64_tr_b16 v[252:253], v212 offset:26432
	s_waitcnt lgkmcnt(6)
	v_mfma_f32_16x16x32_bf16 v[46:49], v[78:81], v[22:25], v[46:49]
	ds_read_b64_tr_b16 v[78:79], v212 offset:17760
	ds_read_b64_tr_b16 v[80:81], v212 offset:26464
	s_waitcnt lgkmcnt(6)
	v_mfma_f32_16x16x32_bf16 v[42:45], v[142:145], v[22:25], v[42:45]
	ds_read_b64_tr_b16 v[142:143], v212 offset:17792
	ds_read_b64_tr_b16 v[144:145], v212 offset:26496
	s_waitcnt lgkmcnt(6)
	v_mfma_f32_16x16x32_bf16 v[38:41], v[244:247], v[22:25], v[38:41]
	ds_read_b64_tr_b16 v[244:245], v212 offset:17824
	ds_read_b64_tr_b16 v[246:247], v212 offset:26528
	s_waitcnt lgkmcnt(6)
	v_mfma_f32_16x16x32_bf16 v[34:37], v[250:253], v[22:25], v[34:37]
	ds_read_b64_tr_b16 v[250:251], v212 offset:17856
	ds_read_b64_tr_b16 v[252:253], v212 offset:26560
	s_waitcnt lgkmcnt(6)
	v_mfma_f32_16x16x32_bf16 v[30:33], v[78:81], v[22:25], v[30:33]
	ds_read_b64_tr_b16 v[78:79], v212 offset:17888
	ds_read_b64_tr_b16 v[80:81], v212 offset:26592
	s_waitcnt lgkmcnt(6)
	v_mfma_f32_16x16x32_bf16 v[26:29], v[142:145], v[22:25], v[26:29]
	s_waitcnt lgkmcnt(4)
	v_mfma_f32_16x16x32_bf16 v[18:21], v[244:247], v[22:25], v[18:21]
	s_waitcnt lgkmcnt(2)
	v_mfma_f32_16x16x32_bf16 v[10:13], v[250:253], v[22:25], v[10:13]
	s_waitcnt lgkmcnt(0)
	v_mfma_f32_16x16x32_bf16 v[2:5], v[78:81], v[22:25], v[2:5]
	s_and_b64 vcc, exec, s[72:73]
	s_cbranch_vccnz .LBB0_570
; __device__ __forceinline__ f32x4 mma16(bf16x8 xrow, bf16x8 ycol, f32x4 c) { return __builtin_amdgcn_mfma_f32_16x16x32_bf16(xrow, ycol, c, 0, 0, 0); }
; __device__ __forceinline__ void p4_ret(Ctx& X, int unit) {
;     ...
; #pragma unroll
;     for (int k2 = 0; k2 < 4; ++k2) if (2 * k2 <= w) {
; #pragma unroll
;         for (int n = 0; n < 16; ++n) { const bf16x8 bf = tr_frag(R2 + (32 * k2) * 544 + (16 * n) * 2 + trp, 16 * 544); acc[n] = mma16(bf, scf[k2], acc[n]); }
;     }
.LBB0_572:
	ds_read_b64_tr_b16 v[78:79], v212 offset:34816
	ds_read_b64_tr_b16 v[80:81], v212 offset:43520
	ds_read_b64_tr_b16 v[244:245], v212 offset:34848
	ds_read_b64_tr_b16 v[246:247], v212 offset:43552
	ds_read_b64_tr_b16 v[250:251], v212 offset:34880
	ds_read_b64_tr_b16 v[252:253], v212 offset:43584
	ds_read_b64_tr_b16 v[22:23], v212 offset:34912
	ds_read_b64_tr_b16 v[24:25], v212 offset:43616
	s_waitcnt lgkmcnt(6)
	v_mfma_f32_16x16x32_bf16 v[74:77], v[78:81], v[14:17], v[74:77]
	ds_read_b64_tr_b16 v[78:79], v212 offset:34944
	ds_read_b64_tr_b16 v[80:81], v212 offset:43648
	s_waitcnt lgkmcnt(6)
	v_mfma_f32_16x16x32_bf16 v[70:73], v[244:247], v[14:17], v[70:73]
	ds_read_b64_tr_b16 v[244:245], v212 offset:34976
	ds_read_b64_tr_b16 v[246:247], v212 offset:43680
	s_waitcnt lgkmcnt(6)
	v_mfma_f32_16x16x32_bf16 v[66:69], v[250:253], v[14:17], v[66:69]
	ds_read_b64_tr_b16 v[250:251], v212 offset:35008
	ds_read_b64_tr_b16 v[252:253], v212 offset:43712
	s_waitcnt lgkmcnt(6)
	v_mfma_f32_16x16x32_bf16 v[62:65], v[22:25], v[14:17], v[62:65]
	ds_read_b64_tr_b16 v[22:23], v212 offset:35040
	ds_read_b64_tr_b16 v[24:25], v212 offset:43744
	s_waitcnt lgkmcnt(6)
	v_mfma_f32_16x16x32_bf16 v[58:61], v[78:81], v[14:17], v[58:61]
	ds_read_b64_tr_b16 v[78:79], v212 offset:35072
	ds_read_b64_tr_b16 v[80:81], v212 offset:43776
	s_waitcnt lgkmcnt(6)
	v_mfma_f32_16x16x32_bf16 v[54:57], v[244:247], v[14:17], v[54:57]
	ds_read_b64_tr_b16 v[244:245], v212 offset:35104
	ds_read_b64_tr_b16 v[246:247], v212 offset:43808
	s_waitcnt lgkmcnt(6)
	v_mfma_f32_16x16x32_bf16 v[50:53], v[250:253], v[14:17], v[50:53]
	ds_read_b64_tr_b16 v[250:251], v212 offset:35136
	ds_read_b64_tr_b16 v[252:253], v212 offset:43840
	s_waitcnt lgkmcnt(6)
	v_mfma_f32_16x16x32_bf16 v[46:49], v[22:25], v[14:17], v[46:49]
	ds_read_b64_tr_b16 v[22:23], v212 offset:35168
	ds_read_b64_tr_b16 v[24:25], v212 offset:43872
	s_waitcnt lgkmcnt(6)
	v_mfma_f32_16x16x32_bf16 v[42:45], v[78:81], v[14:17], v[42:45]
	ds_read_b64_tr_b16 v[78:79], v212 offset:35200
	ds_read_b64_tr_b16 v[80:81], v212 offset:43904
	s_waitcnt lgkmcnt(6)
	v_mfma_f32_16x16x32_bf16 v[38:41], v[244:247], v[14:17], v[38:41]
	ds_read_b64_tr_b16 v[244:245], v212 offset:35232
	ds_read_b64_tr_b16 v[246:247], v212 offset:43936
	s_waitcnt lgkmcnt(6)
	v_mfma_f32_16x16x32_bf16 v[34:37], v[250:253], v[14:17], v[34:37]
	ds_read_b64_tr_b16 v[250:251], v212 offset:35264
	ds_read_b64_tr_b16 v[252:253], v212 offset:43968
	s_waitcnt lgkmcnt(6)
	v_mfma_f32_16x16x32_bf16 v[30:33], v[22:25], v[14:17], v[30:33]
	ds_read_b64_tr_b16 v[22:23], v212 offset:35296
	ds_read_b64_tr_b16 v[24:25], v212 offset:44000
	s_waitcnt lgkmcnt(6)
	v_mfma_f32_16x16x32_bf16 v[26:29], v[78:81], v[14:17], v[26:29]
	s_waitcnt lgkmcnt(4)
	v_mfma_f32_16x16x32_bf16 v[18:21], v[244:247], v[14:17], v[18:21]
	s_waitcnt lgkmcnt(2)
	v_mfma_f32_16x16x32_bf16 v[10:13], v[250:253], v[14:17], v[10:13]
	s_waitcnt lgkmcnt(0)
	v_mfma_f32_16x16x32_bf16 v[2:5], v[22:25], v[14:17], v[2:5]
	s_and_b64 vcc, exec, s[70:71]
	s_cbranch_vccnz .LBB0_533
.LBB0_573:
	ds_read_b64_tr_b16 v[22:23], v212 offset:52224
	ds_read_b64_tr_b16 v[24:25], v212 offset:60928
	ds_read_b64_tr_b16 v[244:245], v212 offset:52256
	ds_read_b64_tr_b16 v[246:247], v212 offset:60960
	ds_read_b64_tr_b16 v[250:251], v212 offset:52288
	ds_read_b64_tr_b16 v[252:253], v212 offset:60992
	ds_read_b64_tr_b16 v[14:15], v212 offset:52320
	ds_read_b64_tr_b16 v[16:17], v212 offset:61024
	s_waitcnt lgkmcnt(6)
	v_mfma_f32_16x16x32_bf16 v[74:77], v[22:25], v[6:9], v[74:77]
	ds_read_b64_tr_b16 v[22:23], v212 offset:52352
	ds_read_b64_tr_b16 v[24:25], v212 offset:61056
	s_waitcnt lgkmcnt(6)
	v_mfma_f32_16x16x32_bf16 v[70:73], v[244:247], v[6:9], v[70:73]
	ds_read_b64_tr_b16 v[244:245], v212 offset:52384
	ds_read_b64_tr_b16 v[246:247], v212 offset:61088
	s_waitcnt lgkmcnt(6)
	v_mfma_f32_16x16x32_bf16 v[66:69], v[250:253], v[6:9], v[66:69]
	ds_read_b64_tr_b16 v[250:251], v212 offset:52416
	ds_read_b64_tr_b16 v[252:253], v212 offset:61120
	s_waitcnt lgkmcnt(6)
	v_mfma_f32_16x16x32_bf16 v[62:65], v[14:17], v[6:9], v[62:65]
	ds_read_b64_tr_b16 v[14:15], v212 offset:52448
	ds_read_b64_tr_b16 v[16:17], v212 offset:61152
	s_waitcnt lgkmcnt(6)
	v_mfma_f32_16x16x32_bf16 v[58:61], v[22:25], v[6:9], v[58:61]
	ds_read_b64_tr_b16 v[22:23], v212 offset:52480
	ds_read_b64_tr_b16 v[24:25], v212 offset:61184
	s_waitcnt lgkmcnt(6)
	v_mfma_f32_16x16x32_bf16 v[54:57], v[244:247], v[6:9], v[54:57]
	ds_read_b64_tr_b16 v[244:245], v212 offset:52512
	ds_read_b64_tr_b16 v[246:247], v212 offset:61216
	s_waitcnt lgkmcnt(6)
	v_mfma_f32_16x16x32_bf16 v[50:53], v[250:253], v[6:9], v[50:53]
	ds_read_b64_tr_b16 v[250:251], v212 offset:52544
	ds_read_b64_tr_b16 v[252:253], v212 offset:61248
	s_waitcnt lgkmcnt(6)
	v_mfma_f32_16x16x32_bf16 v[46:49], v[14:17], v[6:9], v[46:49]
	ds_read_b64_tr_b16 v[14:15], v212 offset:52576
	ds_read_b64_tr_b16 v[16:17], v212 offset:61280
	s_waitcnt lgkmcnt(6)
	v_mfma_f32_16x16x32_bf16 v[42:45], v[22:25], v[6:9], v[42:45]
	ds_read_b64_tr_b16 v[22:23], v212 offset:52608
	ds_read_b64_tr_b16 v[24:25], v212 offset:61312
	s_waitcnt lgkmcnt(6)
	v_mfma_f32_16x16x32_bf16 v[38:41], v[244:247], v[6:9], v[38:41]
	ds_read_b64_tr_b16 v[244:245], v212 offset:52640
	ds_read_b64_tr_b16 v[246:247], v212 offset:61344
	s_waitcnt lgkmcnt(6)
	v_mfma_f32_16x16x32_bf16 v[34:37], v[250:253], v[6:9], v[34:37]
	ds_read_b64_tr_b16 v[250:251], v212 offset:52672
	ds_read_b64_tr_b16 v[252:253], v212 offset:61376
	s_waitcnt lgkmcnt(6)
	v_mfma_f32_16x16x32_bf16 v[30:33], v[14:17], v[6:9], v[30:33]
	ds_read_b64_tr_b16 v[14:15], v212 offset:52704
	ds_read_b64_tr_b16 v[16:17], v212 offset:61408
	s_waitcnt lgkmcnt(6)
	v_mfma_f32_16x16x32_bf16 v[26:29], v[22:25], v[6:9], v[26:29]
	s_waitcnt lgkmcnt(4)
	v_mfma_f32_16x16x32_bf16 v[18:21], v[244:247], v[6:9], v[18:21]
	s_waitcnt lgkmcnt(2)
	v_mfma_f32_16x16x32_bf16 v[10:13], v[250:253], v[6:9], v[10:13]
	s_waitcnt lgkmcnt(0)
	v_mfma_f32_16x16x32_bf16 v[2:5], v[14:17], v[6:9], v[2:5]
	s_branch .LBB0_533

; __global__ void __launch_bounds__(NTHR, 2) fwd(Args args) {
	.amdhsa_kernel _Z3fwd4Args
		.amdhsa_group_segment_fixed_size 0
		.amdhsa_private_segment_fixed_size 0
		.amdhsa_kernarg_size 432
		.amdhsa_user_sgpr_count 2
		.amdhsa_user_sgpr_dispatch_ptr 0
		.amdhsa_user_sgpr_queue_ptr 0
		.amdhsa_user_sgpr_kernarg_segment_ptr 1
		.amdhsa_user_sgpr_dispatch_id 0
		.amdhsa_user_sgpr_kernarg_preload_length 0
		.amdhsa_user_sgpr_kernarg_preload_offset 0
		.amdhsa_user_sgpr_private_segment_size 0
		.amdhsa_uses_dynamic_stack 0
		.amdhsa_enable_private_segment 0
		.amdhsa_system_sgpr_workgroup_id_x 1
		.amdhsa_system_sgpr_workgroup_id_y 0
		.amdhsa_system_sgpr_workgroup_id_z 0
		.amdhsa_system_sgpr_workgroup_info 0
		.amdhsa_system_vgpr_workitem_id 0
		.amdhsa_next_free_vgpr 256
		.amdhsa_next_free_sgpr 98
		.amdhsa_accum_offset 256
		.amdhsa_reserve_vcc 1
		.amdhsa_float_round_mode_32 0
		.amdhsa_float_round_mode_16_64 0
		.amdhsa_float_denorm_mode_32 3
		.amdhsa_float_denorm_mode_16_64 3
		.amdhsa_dx10_clamp 1
		.amdhsa_ieee_mode 1
		.amdhsa_fp16_overflow 0
		.amdhsa_tg_split 0
		.amdhsa_exception_fp_ieee_invalid_op 0
		.amdhsa_exception_fp_denorm_src 0
		.amdhsa_exception_fp_ieee_div_zero 0
		.amdhsa_exception_fp_ieee_overflow 0
		.amdhsa_exception_fp_ieee_underflow 0
		.amdhsa_exception_fp_ieee_inexact 0
		.amdhsa_exception_int_div_zero 0
	.end_amdhsa_kernel

; __global__ void __launch_bounds__(NTHR, 2) fwd(Args args) {
amdhsa.kernels:
  - .agpr_count:     0
    .args:
      - .offset:         0
        .size:           176
        .value_kind:     by_value
      - .offset:         176
        .size:           4
        .value_kind:     hidden_block_count_x
      - .offset:         180
        .size:           4
        .value_kind:     hidden_block_count_y
      - .offset:         184
        .size:           4
        .value_kind:     hidden_block_count_z
      - .offset:         188
        .size:           2
        .value_kind:     hidden_group_size_x
      - .offset:         190
        .size:           2
        .value_kind:     hidden_group_size_y
      - .offset:         192
        .size:           2
        .value_kind:     hidden_group_size_z
      - .offset:         194
        .size:           2
        .value_kind:     hidden_remainder_x
      - .offset:         196
        .size:           2
        .value_kind:     hidden_remainder_y
      - .offset:         198
        .size:           2
        .value_kind:     hidden_remainder_z
      - .offset:         216
        .size:           8
        .value_kind:     hidden_global_offset_x
      - .offset:         224
        .size:           8
        .value_kind:     hidden_global_offset_y
      - .offset:         232
        .size:           8
        .value_kind:     hidden_global_offset_z
      - .offset:         240
        .size:           2
        .value_kind:     hidden_grid_dims
      - .offset:         296
        .size:           4
        .value_kind:     hidden_dynamic_lds_size
    .group_segment_fixed_size: 0
    .kernarg_segment_align: 8
    .kernarg_segment_size: 432
    .language:       OpenCL C
    .language_version:
      - 2
      - 0
    .max_flat_workgroup_size: 512
    .name:           _Z3fwd4Args
    .private_segment_fixed_size: 0
    .sgpr_count:     104
    .sgpr_spill_count: 59
    .symbol:         _Z3fwd4Args.kd
    .uniform_work_group_size: 1
    .uses_dynamic_stack: false
    .vgpr_count:     256
    .vgpr_spill_count: 0
    .wavefront_size: 64
